# attention loops unrolled by ring slot + MoE GEMM1 first K-trip peeled with C=0 (no accumulator zeroing moves)
# speedup vs baseline: 1.0714x; 1.0120x over previous
.Lfd0_entry:
	v_add_u32_e32 v232, s91, v222
	v_add_u32_e32 v233, s91, v221
	s_add_i32 s32, s86, s2
	s_add_i32 s50, s32, -1
	s_mov_b32 s51, 0
	s_lshl_b64 s[50:51], s[50:51], 6
	s_add_u32 s50, s97, s50
	s_addc_u32 s51, s87, s51
	s_add_i32 s10, s32, -3
	s_cmp_lt_u32 s10, 61
	s_cselect_b32 s10, s90, s17
	s_add_i32 s48, s10, s3
	s_ashr_i32 s49, s48, 31
	s_lshl_b64 s[48:49], s[48:49], 10
	s_add_u32 s48, s95, s48
	s_addc_u32 s49, s96, s49
	s_add_i32 m0, s79, 0x1000
	s_nop 0
	global_load_lds_dwordx4 v209, s[48:49]
	s_add_i32 m0, s79, 0x4000
	s_nop 0
	global_load_lds_dwordx4 v218, s[50:51]
	ds_read_b128 v[144:147], v232 offset:8192
	ds_read_b128 v[148:151], v233 offset:8192
	ds_read_b128 v[152:155], v232 offset:10240
	ds_read_b128 v[156:159], v233 offset:10240
	ds_read_b128 v[176:179], v232 offset:24576
	ds_read_b128 v[180:183], v233 offset:24576
	ds_read_b128 v[168:171], v232 offset:26624
	ds_read_b128 v[172:175], v233 offset:26624
	ds_read_b128 v[192:195], v232 offset:28672
	ds_read_b128 v[196:199], v233 offset:28672
	ds_read_b128 v[184:187], v232 offset:30720
	ds_read_b128 v[188:191], v233 offset:30720
	s_add_i32 s32, s86, s2
	s_add_i32 s32, s32, 1
	s_add_i32 s50, s32, -1
	s_mov_b32 s51, 0
	s_lshl_b64 s[50:51], s[50:51], 6
	s_add_u32 s50, s97, s50
	s_addc_u32 s51, s87, s51
	s_add_i32 s10, s32, -3
	s_cmp_lt_u32 s10, 61
	s_cselect_b32 s10, s90, s17
	s_add_i32 s48, s10, s3
	s_add_i32 s48, s48, 64
	s_ashr_i32 s49, s48, 31
	s_lshl_b64 s[48:49], s[48:49], 10
	s_add_u32 s48, s95, s48
	s_addc_u32 s49, s96, s49
	s_waitcnt vmcnt(4)
	s_waitcnt lgkmcnt(0)
	s_barrier
	s_mov_b32 s13, s12
	s_add_i32 s12, s12, 1
	s_and_b32 s12, s12, 3
	s_add_i32 s2, s2, 1
	s_add_i32 s3, s3, 64
	s_cmp_lt_u32 s2, s16
	s_cbranch_scc0 .Lfd0_drainA
.Lfd0_it3:
	v_mfma_scale_f32_32x32x64_f8f6f4 v[96:111], v[144:151], v[128:135], v[80:95], v220, v220 op_sel_hi:[0,0,0]
	s_add_i32 m0, s79, 0x2000
	s_nop 0
	global_load_lds_dwordx4 v209, s[48:49]
	s_add_i32 m0, s79, 0x6000
	s_nop 0
	global_load_lds_dwordx4 v218, s[50:51]
	s_add_i32 s32, s86, s2
	s_add_i32 s32, s32, 1
	s_add_i32 s50, s32, -1
	s_mov_b32 s51, 0
	s_lshl_b64 s[50:51], s[50:51], 6
	s_add_u32 s50, s97, s50
	s_addc_u32 s51, s87, s51
	s_add_i32 s10, s32, -3
	v_mfma_scale_f32_32x32x64_f8f6f4 v[112:127], v[152:159], v[128:135], v[80:95], v220, v220 op_sel_hi:[0,0,0]
	s_cmp_lt_u32 s10, 61
	s_cselect_b32 s10, s90, s17
	s_add_i32 s48, s10, s3
	s_add_i32 s48, s48, 64
	s_ashr_i32 s49, s48, 31
	s_lshl_b64 s[48:49], s[48:49], 10
	s_add_u32 s48, s95, s48
	s_addc_u32 s49, s96, s49
	v_mfma_scale_f32_32x32x64_f8f6f4 v[0:15], v[160:167], v[136:143], v[0:15], v219, v219 op_sel_hi:[0,0,0]
	ds_read_b128 v[144:147], v232 offset:12288
	ds_read_b128 v[148:151], v233 offset:12288
	ds_read_b128 v[152:155], v232 offset:14336
	ds_read_b128 v[156:159], v233 offset:14336
	v_max3_f32 v226, v96, v97, v98
	v_max3_f32 v202, v99, v100, v101
	v_max3_f32 v203, v102, v103, v104
	v_max3_f32 v211, v105, v106, v107
	v_max3_f32 v226, v226, v108, v109
	v_max3_f32 v202, v202, v110, v111
	v_max3_f32 v226, v226, v203, v211
	v_max_f32_e32 v226, v226, v202
	v_mfma_scale_f32_32x32x64_f8f6f4 v[64:79], v[160:167], v[176:183], v[64:79], v219, v219 op_sel_hi:[0,0,0]
	v_max3_f32 v227, v112, v113, v114
	v_max3_f32 v202, v115, v116, v117
	v_max3_f32 v203, v118, v119, v120
	v_max3_f32 v211, v121, v122, v123
	v_max3_f32 v227, v227, v124, v125
	v_max3_f32 v202, v202, v126, v127
	v_max3_f32 v227, v227, v203, v211
	v_max_f32_e32 v227, v227, v202
	v_max_f32_e32 v226, v226, v227
	v_cmp_lt_f32_e32 vcc, 0x41000000, v226
	s_cbranch_vccnz .Lfd0_3_rare
	v_mfma_scale_f32_32x32x64_f8f6f4 v[48:63], v[160:167], v[168:175], v[48:63], v219, v219 op_sel_hi:[0,0,0]
	ds_read_b128 v[176:179], v232 offset:32768
	ds_read_b128 v[180:183], v233 offset:32768
	v_exp_f32_e32 v96, v96
	v_exp_f32_e32 v112, v112
	v_exp_f32_e32 v97, v97
	v_exp_f32_e32 v113, v113
	v_exp_f32_e32 v100, v100
	v_exp_f32_e32 v116, v116
	v_exp_f32_e32 v101, v101
	v_exp_f32_e32 v117, v117
	v_mfma_scale_f32_32x32x64_f8f6f4 v[32:47], v[160:167], v[192:199], v[32:47], v219, v219 op_sel_hi:[0,0,0]
	ds_read_b128 v[168:171], v232 offset:34816
	ds_read_b128 v[172:175], v233 offset:34816
	v_exp_f32_e32 v104, v104
	v_exp_f32_e32 v120, v120
	v_exp_f32_e32 v105, v105
	v_exp_f32_e32 v121, v121
	v_exp_f32_e32 v108, v108
	v_exp_f32_e32 v124, v124
	v_exp_f32_e32 v109, v109
	v_exp_f32_e32 v125, v125
	v_mfma_scale_f32_32x32x64_f8f6f4 v[16:31], v[160:167], v[184:191], v[16:31], v219, v219 op_sel_hi:[0,0,0]
	ds_read_b128 v[192:195], v232 offset:36864
	ds_read_b128 v[196:199], v233 offset:36864
	v_exp_f32_e32 v98, v98
	v_exp_f32_e32 v114, v114
	v_exp_f32_e32 v99, v99
	v_exp_f32_e32 v115, v115
	v_exp_f32_e32 v102, v102
	v_exp_f32_e32 v118, v118
	v_exp_f32_e32 v103, v103
	v_exp_f32_e32 v119, v119
	ds_read_b128 v[184:187], v232 offset:38912
	ds_read_b128 v[188:191], v233 offset:38912
.Lfd0_3_join:
	v_exp_f32_e32 v106, v106
	v_exp_f32_e32 v122, v122
	v_exp_f32_e32 v107, v107
	v_exp_f32_e32 v123, v123
	v_exp_f32_e32 v110, v110
	v_exp_f32_e32 v126, v126
	v_exp_f32_e32 v111, v111
	v_exp_f32_e32 v127, v127
	v_cvt_pk_fp8_f32 v236, v96, v97
	v_cvt_pk_fp8_f32 v240, v112, v113
	v_cvt_pk_fp8_f32 v237, v100, v101
	v_cvt_pk_fp8_f32 v241, v116, v117
	v_cvt_pk_fp8_f32 v238, v104, v105
	v_cvt_pk_fp8_f32 v242, v120, v121
	v_cvt_pk_fp8_f32 v239, v108, v109
	v_cvt_pk_fp8_f32 v243, v124, v125
	v_cvt_pk_fp8_f32 v236, v98, v99 op_sel:[0,0,1]
	v_cvt_pk_fp8_f32 v240, v114, v115 op_sel:[0,0,1]
	v_cvt_pk_fp8_f32 v237, v102, v103 op_sel:[0,0,1]
	v_cvt_pk_fp8_f32 v241, v118, v119 op_sel:[0,0,1]
	v_cvt_pk_fp8_f32 v238, v106, v107 op_sel:[0,0,1]
	v_cvt_pk_fp8_f32 v242, v122, v123 op_sel:[0,0,1]
	v_cvt_pk_fp8_f32 v239, v110, v111 op_sel:[0,0,1]
	v_cvt_pk_fp8_f32 v243, v126, v127 op_sel:[0,0,1]
	s_waitcnt vmcnt(4)
	s_waitcnt lgkmcnt(0)
	s_barrier
	s_mov_b32 s13, s12
	s_add_i32 s12, s12, 1
	s_and_b32 s12, s12, 3
	s_add_i32 s2, s2, 1
	s_add_i32 s3, s3, 64
	s_cmp_lt_u32 s2, s16
	s_cbranch_scc1 .Lfd0_it0
	s_branch .Lfd0_drainB
.Lfd0_it0:
	v_mfma_scale_f32_32x32x64_f8f6f4 v[96:111], v[144:151], v[128:135], v[80:95], v220, v220 op_sel_hi:[0,0,0]
	s_add_i32 m0, s79, 0x3000
	s_nop 0
	global_load_lds_dwordx4 v209, s[48:49]
	s_add_i32 m0, s79, 0x8000
	s_nop 0
	global_load_lds_dwordx4 v218, s[50:51]
	s_add_i32 s32, s86, s2
	s_add_i32 s32, s32, 1
	s_add_i32 s50, s32, -1
	s_mov_b32 s51, 0
	s_lshl_b64 s[50:51], s[50:51], 6
	s_add_u32 s50, s97, s50
	s_addc_u32 s51, s87, s51
	s_add_i32 s10, s32, -3
	v_mfma_scale_f32_32x32x64_f8f6f4 v[112:127], v[152:159], v[128:135], v[80:95], v220, v220 op_sel_hi:[0,0,0]
	s_cmp_lt_u32 s10, 61
	s_cselect_b32 s10, s90, s17
	s_add_i32 s48, s10, s3
	s_add_i32 s48, s48, 64
	s_ashr_i32 s49, s48, 31
	s_lshl_b64 s[48:49], s[48:49], 10
	s_add_u32 s48, s95, s48
	s_addc_u32 s49, s96, s49
	v_mfma_scale_f32_32x32x64_f8f6f4 v[0:15], v[236:243], v[136:143], v[0:15], v219, v219 op_sel_hi:[0,0,0]
	ds_read_b128 v[144:147], v232
	ds_read_b128 v[148:151], v233
	ds_read_b128 v[152:155], v232 offset:2048
	ds_read_b128 v[156:159], v233 offset:2048
	v_max3_f32 v226, v96, v97, v98
	v_max3_f32 v202, v99, v100, v101
	v_max3_f32 v203, v102, v103, v104
	v_max3_f32 v211, v105, v106, v107
	v_max3_f32 v226, v226, v108, v109
	v_max3_f32 v202, v202, v110, v111
	v_max3_f32 v226, v226, v203, v211
	v_max_f32_e32 v226, v226, v202
	v_mfma_scale_f32_32x32x64_f8f6f4 v[64:79], v[236:243], v[176:183], v[64:79], v219, v219 op_sel_hi:[0,0,0]
	v_max3_f32 v227, v112, v113, v114
	v_max3_f32 v202, v115, v116, v117
	v_max3_f32 v203, v118, v119, v120
	v_max3_f32 v211, v121, v122, v123
	v_max3_f32 v227, v227, v124, v125
	v_max3_f32 v202, v202, v126, v127
	v_max3_f32 v227, v227, v203, v211
	v_max_f32_e32 v227, v227, v202
	v_max_f32_e32 v226, v226, v227
	v_cmp_lt_f32_e32 vcc, 0x41000000, v226
	s_cbranch_vccnz .Lfd0_0_rare
	v_mfma_scale_f32_32x32x64_f8f6f4 v[48:63], v[236:243], v[168:175], v[48:63], v219, v219 op_sel_hi:[0,0,0]
	ds_read_b128 v[176:179], v232 offset:40960
	ds_read_b128 v[180:183], v233 offset:40960
	v_exp_f32_e32 v96, v96
	v_exp_f32_e32 v112, v112
	v_exp_f32_e32 v97, v97
	v_exp_f32_e32 v113, v113
	v_exp_f32_e32 v100, v100
	v_exp_f32_e32 v116, v116
	v_exp_f32_e32 v101, v101
	v_exp_f32_e32 v117, v117
	v_mfma_scale_f32_32x32x64_f8f6f4 v[32:47], v[236:243], v[192:199], v[32:47], v219, v219 op_sel_hi:[0,0,0]
	ds_read_b128 v[168:171], v232 offset:43008
	ds_read_b128 v[172:175], v233 offset:43008
	v_exp_f32_e32 v104, v104
	v_exp_f32_e32 v120, v120
	v_exp_f32_e32 v105, v105
	v_exp_f32_e32 v121, v121
	v_exp_f32_e32 v108, v108
	v_exp_f32_e32 v124, v124
	v_exp_f32_e32 v109, v109
	v_exp_f32_e32 v125, v125
	v_mfma_scale_f32_32x32x64_f8f6f4 v[16:31], v[236:243], v[184:191], v[16:31], v219, v219 op_sel_hi:[0,0,0]
	ds_read_b128 v[192:195], v232 offset:45056
	ds_read_b128 v[196:199], v233 offset:45056
	v_exp_f32_e32 v98, v98
	v_exp_f32_e32 v114, v114
	v_exp_f32_e32 v99, v99
	v_exp_f32_e32 v115, v115
	v_exp_f32_e32 v102, v102
	v_exp_f32_e32 v118, v118
	v_exp_f32_e32 v103, v103
	v_exp_f32_e32 v119, v119
	ds_read_b128 v[184:187], v232 offset:47104
	ds_read_b128 v[188:191], v233 offset:47104

.Lfd0_it1:
	v_mfma_scale_f32_32x32x64_f8f6f4 v[96:111], v[144:151], v[128:135], v[80:95], v220, v220 op_sel_hi:[0,0,0]
	s_add_i32 m0, s79, 0x0
	s_nop 0
	global_load_lds_dwordx4 v209, s[48:49]
	s_add_i32 m0, s79, 0xa000
	s_nop 0
	global_load_lds_dwordx4 v218, s[50:51]
	s_add_i32 s32, s86, s2
	s_add_i32 s32, s32, 1
	s_add_i32 s50, s32, -1
	s_mov_b32 s51, 0
	s_lshl_b64 s[50:51], s[50:51], 6
	s_add_u32 s50, s97, s50
	s_addc_u32 s51, s87, s51
	s_add_i32 s10, s32, -3
	v_mfma_scale_f32_32x32x64_f8f6f4 v[112:127], v[152:159], v[128:135], v[80:95], v220, v220 op_sel_hi:[0,0,0]
	s_cmp_lt_u32 s10, 61
	s_cselect_b32 s10, s90, s17
	s_add_i32 s48, s10, s3
	s_add_i32 s48, s48, 64
	s_ashr_i32 s49, s48, 31
	s_lshl_b64 s[48:49], s[48:49], 10
	s_add_u32 s48, s95, s48
	s_addc_u32 s49, s96, s49
	v_mfma_scale_f32_32x32x64_f8f6f4 v[0:15], v[160:167], v[136:143], v[0:15], v219, v219 op_sel_hi:[0,0,0]
	ds_read_b128 v[144:147], v232 offset:4096
	ds_read_b128 v[148:151], v233 offset:4096
	ds_read_b128 v[152:155], v232 offset:6144
	ds_read_b128 v[156:159], v233 offset:6144
	v_max3_f32 v226, v96, v97, v98
	v_max3_f32 v202, v99, v100, v101
	v_max3_f32 v203, v102, v103, v104
	v_max3_f32 v211, v105, v106, v107
	v_max3_f32 v226, v226, v108, v109
	v_max3_f32 v202, v202, v110, v111
	v_max3_f32 v226, v226, v203, v211
	v_max_f32_e32 v226, v226, v202
	v_mfma_scale_f32_32x32x64_f8f6f4 v[64:79], v[160:167], v[176:183], v[64:79], v219, v219 op_sel_hi:[0,0,0]
	v_max3_f32 v227, v112, v113, v114
	v_max3_f32 v202, v115, v116, v117
	v_max3_f32 v203, v118, v119, v120
	v_max3_f32 v211, v121, v122, v123
	v_max3_f32 v227, v227, v124, v125
	v_max3_f32 v202, v202, v126, v127
	v_max3_f32 v227, v227, v203, v211
	v_max_f32_e32 v227, v227, v202
	v_max_f32_e32 v226, v226, v227
	v_cmp_lt_f32_e32 vcc, 0x41000000, v226
	s_cbranch_vccnz .Lfd0_1_rare
	v_mfma_scale_f32_32x32x64_f8f6f4 v[48:63], v[160:167], v[168:175], v[48:63], v219, v219 op_sel_hi:[0,0,0]
	ds_read_b128 v[176:179], v232 offset:16384
	ds_read_b128 v[180:183], v233 offset:16384
	v_exp_f32_e32 v96, v96
	v_exp_f32_e32 v112, v112
	v_exp_f32_e32 v97, v97
	v_exp_f32_e32 v113, v113
	v_exp_f32_e32 v100, v100
	v_exp_f32_e32 v116, v116
	v_exp_f32_e32 v101, v101
	v_exp_f32_e32 v117, v117
	v_mfma_scale_f32_32x32x64_f8f6f4 v[32:47], v[160:167], v[192:199], v[32:47], v219, v219 op_sel_hi:[0,0,0]
	ds_read_b128 v[168:171], v232 offset:18432
	ds_read_b128 v[172:175], v233 offset:18432
	v_exp_f32_e32 v104, v104
	v_exp_f32_e32 v120, v120
	v_exp_f32_e32 v105, v105
	v_exp_f32_e32 v121, v121
	v_exp_f32_e32 v108, v108
	v_exp_f32_e32 v124, v124
	v_exp_f32_e32 v109, v109
	v_exp_f32_e32 v125, v125
	v_mfma_scale_f32_32x32x64_f8f6f4 v[16:31], v[160:167], v[184:191], v[16:31], v219, v219 op_sel_hi:[0,0,0]
	ds_read_b128 v[192:195], v232 offset:20480
	ds_read_b128 v[196:199], v233 offset:20480
	v_exp_f32_e32 v98, v98
	v_exp_f32_e32 v114, v114
	v_exp_f32_e32 v99, v99
	v_exp_f32_e32 v115, v115
	v_exp_f32_e32 v102, v102
	v_exp_f32_e32 v118, v118
	v_exp_f32_e32 v103, v103
	v_exp_f32_e32 v119, v119
	ds_read_b128 v[184:187], v232 offset:22528
	ds_read_b128 v[188:191], v233 offset:22528

.Lfd0_it2:
	v_mfma_scale_f32_32x32x64_f8f6f4 v[96:111], v[144:151], v[128:135], v[80:95], v220, v220 op_sel_hi:[0,0,0]
	s_add_i32 m0, s79, 0x1000
	s_nop 0
	global_load_lds_dwordx4 v209, s[48:49]
	s_add_i32 m0, s79, 0x4000
	s_nop 0
	global_load_lds_dwordx4 v218, s[50:51]
	s_add_i32 s32, s86, s2
	s_add_i32 s32, s32, 1
	s_add_i32 s50, s32, -1
	s_mov_b32 s51, 0
	s_lshl_b64 s[50:51], s[50:51], 6
	s_add_u32 s50, s97, s50
	s_addc_u32 s51, s87, s51
	s_add_i32 s10, s32, -3
	v_mfma_scale_f32_32x32x64_f8f6f4 v[112:127], v[152:159], v[128:135], v[80:95], v220, v220 op_sel_hi:[0,0,0]
	s_cmp_lt_u32 s10, 61
	s_cselect_b32 s10, s90, s17
	s_add_i32 s48, s10, s3
	s_add_i32 s48, s48, 64
	s_ashr_i32 s49, s48, 31
	s_lshl_b64 s[48:49], s[48:49], 10
	s_add_u32 s48, s95, s48
	s_addc_u32 s49, s96, s49
	v_mfma_scale_f32_32x32x64_f8f6f4 v[0:15], v[236:243], v[136:143], v[0:15], v219, v219 op_sel_hi:[0,0,0]
	ds_read_b128 v[144:147], v232 offset:8192
	ds_read_b128 v[148:151], v233 offset:8192
	ds_read_b128 v[152:155], v232 offset:10240
	ds_read_b128 v[156:159], v233 offset:10240
	v_max3_f32 v226, v96, v97, v98
	v_max3_f32 v202, v99, v100, v101
	v_max3_f32 v203, v102, v103, v104
	v_max3_f32 v211, v105, v106, v107
	v_max3_f32 v226, v226, v108, v109
	v_max3_f32 v202, v202, v110, v111
	v_max3_f32 v226, v226, v203, v211
	v_max_f32_e32 v226, v226, v202
	v_mfma_scale_f32_32x32x64_f8f6f4 v[64:79], v[236:243], v[176:183], v[64:79], v219, v219 op_sel_hi:[0,0,0]
	v_max3_f32 v227, v112, v113, v114
	v_max3_f32 v202, v115, v116, v117
	v_max3_f32 v203, v118, v119, v120
	v_max3_f32 v211, v121, v122, v123
	v_max3_f32 v227, v227, v124, v125
	v_max3_f32 v202, v202, v126, v127
	v_max3_f32 v227, v227, v203, v211
	v_max_f32_e32 v227, v227, v202
	v_max_f32_e32 v226, v226, v227
	v_cmp_lt_f32_e32 vcc, 0x41000000, v226
	s_cbranch_vccnz .Lfd0_2_rare
	v_mfma_scale_f32_32x32x64_f8f6f4 v[48:63], v[236:243], v[168:175], v[48:63], v219, v219 op_sel_hi:[0,0,0]
	ds_read_b128 v[176:179], v232 offset:24576
	ds_read_b128 v[180:183], v233 offset:24576
	v_exp_f32_e32 v96, v96
	v_exp_f32_e32 v112, v112
	v_exp_f32_e32 v97, v97
	v_exp_f32_e32 v113, v113
	v_exp_f32_e32 v100, v100
	v_exp_f32_e32 v116, v116
	v_exp_f32_e32 v101, v101
	v_exp_f32_e32 v117, v117
	v_mfma_scale_f32_32x32x64_f8f6f4 v[32:47], v[236:243], v[192:199], v[32:47], v219, v219 op_sel_hi:[0,0,0]
	ds_read_b128 v[168:171], v232 offset:26624
	ds_read_b128 v[172:175], v233 offset:26624
	v_exp_f32_e32 v104, v104
	v_exp_f32_e32 v120, v120
	v_exp_f32_e32 v105, v105
	v_exp_f32_e32 v121, v121
	v_exp_f32_e32 v108, v108
	v_exp_f32_e32 v124, v124
	v_exp_f32_e32 v109, v109
	v_exp_f32_e32 v125, v125
	v_mfma_scale_f32_32x32x64_f8f6f4 v[16:31], v[236:243], v[184:191], v[16:31], v219, v219 op_sel_hi:[0,0,0]
	ds_read_b128 v[192:195], v232 offset:28672
	ds_read_b128 v[196:199], v233 offset:28672
	v_exp_f32_e32 v98, v98
	v_exp_f32_e32 v114, v114
	v_exp_f32_e32 v99, v99
	v_exp_f32_e32 v115, v115
	v_exp_f32_e32 v102, v102
	v_exp_f32_e32 v118, v118
	v_exp_f32_e32 v103, v103
	v_exp_f32_e32 v119, v119
	ds_read_b128 v[184:187], v232 offset:30720
	ds_read_b128 v[188:191], v233 offset:30720

.Lfd0_drainA:
	v_mfma_scale_f32_32x32x64_f8f6f4 v[96:111], v[144:151], v[128:135], v[80:95], v220, v220 op_sel_hi:[0,0,0]
	v_mfma_scale_f32_32x32x64_f8f6f4 v[112:127], v[152:159], v[128:135], v[80:95], v220, v220 op_sel_hi:[0,0,0]
	v_mfma_scale_f32_32x32x64_f8f6f4 v[0:15], v[160:167], v[136:143], v[0:15], v219, v219 op_sel_hi:[0,0,0]
	v_max3_f32 v226, v96, v97, v98
	v_max3_f32 v202, v99, v100, v101
	v_max3_f32 v203, v102, v103, v104
	v_max3_f32 v211, v105, v106, v107
	v_max3_f32 v226, v226, v108, v109
	v_max3_f32 v202, v202, v110, v111
	v_max3_f32 v226, v226, v203, v211
	v_max_f32_e32 v226, v226, v202
	v_mfma_scale_f32_32x32x64_f8f6f4 v[64:79], v[160:167], v[176:183], v[64:79], v219, v219 op_sel_hi:[0,0,0]
	v_max3_f32 v227, v112, v113, v114
	v_max3_f32 v202, v115, v116, v117
	v_max3_f32 v203, v118, v119, v120
	v_max3_f32 v211, v121, v122, v123
	v_max3_f32 v227, v227, v124, v125
	v_max3_f32 v202, v202, v126, v127
	v_max3_f32 v227, v227, v203, v211
	v_max_f32_e32 v227, v227, v202
	v_max_f32_e32 v226, v226, v227
	v_cmp_lt_f32_e32 vcc, 0x41000000, v226
	s_cbranch_vccnz .Lfd0dA_rare
	v_mfma_scale_f32_32x32x64_f8f6f4 v[48:63], v[160:167], v[168:175], v[48:63], v219, v219 op_sel_hi:[0,0,0]
	v_exp_f32_e32 v96, v96
	v_exp_f32_e32 v112, v112
	v_exp_f32_e32 v97, v97
	v_exp_f32_e32 v113, v113
	v_exp_f32_e32 v100, v100
	v_exp_f32_e32 v116, v116
	v_exp_f32_e32 v101, v101
	v_exp_f32_e32 v117, v117
	v_mfma_scale_f32_32x32x64_f8f6f4 v[32:47], v[160:167], v[192:199], v[32:47], v219, v219 op_sel_hi:[0,0,0]
	v_exp_f32_e32 v104, v104
	v_exp_f32_e32 v120, v120
	v_exp_f32_e32 v105, v105
	v_exp_f32_e32 v121, v121
	v_exp_f32_e32 v108, v108
	v_exp_f32_e32 v124, v124
	v_exp_f32_e32 v109, v109
	v_exp_f32_e32 v125, v125
	v_mfma_scale_f32_32x32x64_f8f6f4 v[16:31], v[160:167], v[184:191], v[16:31], v219, v219 op_sel_hi:[0,0,0]
	v_exp_f32_e32 v98, v98
	v_exp_f32_e32 v114, v114
	v_exp_f32_e32 v99, v99
	v_exp_f32_e32 v115, v115
	v_exp_f32_e32 v102, v102
	v_exp_f32_e32 v118, v118
	v_exp_f32_e32 v103, v103
	v_exp_f32_e32 v119, v119

.Lfd0_drainB:
	v_mfma_scale_f32_32x32x64_f8f6f4 v[96:111], v[144:151], v[128:135], v[80:95], v220, v220 op_sel_hi:[0,0,0]
	v_mfma_scale_f32_32x32x64_f8f6f4 v[112:127], v[152:159], v[128:135], v[80:95], v220, v220 op_sel_hi:[0,0,0]
	v_mfma_scale_f32_32x32x64_f8f6f4 v[0:15], v[236:243], v[136:143], v[0:15], v219, v219 op_sel_hi:[0,0,0]
	v_max3_f32 v226, v96, v97, v98
	v_max3_f32 v202, v99, v100, v101
	v_max3_f32 v203, v102, v103, v104
	v_max3_f32 v211, v105, v106, v107
	v_max3_f32 v226, v226, v108, v109
	v_max3_f32 v202, v202, v110, v111
	v_max3_f32 v226, v226, v203, v211
	v_max_f32_e32 v226, v226, v202
	v_mfma_scale_f32_32x32x64_f8f6f4 v[64:79], v[236:243], v[176:183], v[64:79], v219, v219 op_sel_hi:[0,0,0]
	v_max3_f32 v227, v112, v113, v114
	v_max3_f32 v202, v115, v116, v117
	v_max3_f32 v203, v118, v119, v120
	v_max3_f32 v211, v121, v122, v123
	v_max3_f32 v227, v227, v124, v125
	v_max3_f32 v202, v202, v126, v127
	v_max3_f32 v227, v227, v203, v211
	v_max_f32_e32 v227, v227, v202
	v_max_f32_e32 v226, v226, v227
	v_cmp_lt_f32_e32 vcc, 0x41000000, v226
	s_cbranch_vccnz .Lfd0dB_rare
	v_mfma_scale_f32_32x32x64_f8f6f4 v[48:63], v[236:243], v[168:175], v[48:63], v219, v219 op_sel_hi:[0,0,0]
	v_exp_f32_e32 v96, v96
	v_exp_f32_e32 v112, v112
	v_exp_f32_e32 v97, v97
	v_exp_f32_e32 v113, v113
	v_exp_f32_e32 v100, v100
	v_exp_f32_e32 v116, v116
	v_exp_f32_e32 v101, v101
	v_exp_f32_e32 v117, v117
	v_mfma_scale_f32_32x32x64_f8f6f4 v[32:47], v[236:243], v[192:199], v[32:47], v219, v219 op_sel_hi:[0,0,0]
	v_exp_f32_e32 v104, v104
	v_exp_f32_e32 v120, v120
	v_exp_f32_e32 v105, v105
	v_exp_f32_e32 v121, v121
	v_exp_f32_e32 v108, v108
	v_exp_f32_e32 v124, v124
	v_exp_f32_e32 v109, v109
	v_exp_f32_e32 v125, v125
	v_mfma_scale_f32_32x32x64_f8f6f4 v[16:31], v[236:243], v[184:191], v[16:31], v219, v219 op_sel_hi:[0,0,0]
	v_exp_f32_e32 v98, v98
	v_exp_f32_e32 v114, v114
	v_exp_f32_e32 v99, v99
	v_exp_f32_e32 v115, v115
	v_exp_f32_e32 v102, v102
	v_exp_f32_e32 v118, v118
	v_exp_f32_e32 v103, v103
	v_exp_f32_e32 v119, v119

.Lfd0_3_rare:
	v_mfma_scale_f32_32x32x64_f8f6f4 v[48:63], v[160:167], v[168:175], v[48:63], v219, v219 op_sel_hi:[0,0,0]
	ds_read_b128 v[176:179], v232 offset:32768
	ds_read_b128 v[180:183], v233 offset:32768
	v_mfma_scale_f32_32x32x64_f8f6f4 v[32:47], v[160:167], v[192:199], v[32:47], v219, v219 op_sel_hi:[0,0,0]
	ds_read_b128 v[168:171], v232 offset:34816
	ds_read_b128 v[172:175], v233 offset:34816
	v_mfma_scale_f32_32x32x64_f8f6f4 v[16:31], v[160:167], v[184:191], v[16:31], v219, v219 op_sel_hi:[0,0,0]
	ds_read_b128 v[192:195], v232 offset:36864
	ds_read_b128 v[196:199], v233 offset:36864
	s_nop 15
	s_nop 15
	s_nop 15
	s_nop 15
	s_nop 15
	ds_read_b128 v[184:187], v232 offset:38912
	ds_read_b128 v[188:191], v233 offset:38912
	v_mov_b32_e32 v227, v226
	s_nop 1
	v_permlane32_swap_b32_e32 v226, v227
	v_max3_f32 v226, v226, v227, v227
	s_nop 0
	v_max_f32_e32 v80, v226, v226
	v_max_f32_e32 v82, 0, v80
	s_and_saveexec_b64 s[0:1], s[6:7]
	v_exp_f32_e64 v80, -v82
	s_nop 0
	ds_write_b32 v223, v80 offset:49152
	s_or_b64 exec, exec, s[0:1]
	v_add_u32_e32 v210, s78, v224
	s_waitcnt lgkmcnt(0)
	v_add_u32_e32 v251, 0xc000, v210
	ds_read2_b32 v[228:229], v251 offset1:1
	v_add_u32_e32 v251, 0xc008, v210
	ds_read2_b32 v[230:231], v251 offset1:1
	v_add_u32_e32 v251, 0xc020, v210
	ds_read2_b32 v[244:245], v251 offset1:1
	v_add_u32_e32 v251, 0xc028, v210
	ds_read2_b32 v[246:247], v251 offset1:1
	v_add_u32_e32 v251, 0xc040, v210
	ds_read2_b32 v[248:249], v251 offset1:1
	v_add_u32_e32 v251, 0xc048, v210
	ds_read2_b32 v[206:207], v251 offset1:1
	v_add_u32_e32 v251, 0xc060, v210
	ds_read2_b32 v[252:253], v251 offset1:1
	v_add_u32_e32 v251, 0xc068, v210
	ds_read2_b32 v[202:203], v251 offset1:1
	v_add_f32_e32 v225, v225, v82
	v_xor_b32_e32 v80, 0x80000000, v225
	v_pk_add_f32 v[96:97], v[96:97], v[82:83] op_sel_hi:[1,0] neg_lo:[0,1] neg_hi:[0,1]
	v_pk_add_f32 v[112:113], v[112:113], v[82:83] op_sel_hi:[1,0] neg_lo:[0,1] neg_hi:[0,1]
	v_pk_add_f32 v[98:99], v[98:99], v[82:83] op_sel_hi:[1,0] neg_lo:[0,1] neg_hi:[0,1]
	v_pk_add_f32 v[114:115], v[114:115], v[82:83] op_sel_hi:[1,0] neg_lo:[0,1] neg_hi:[0,1]
	v_pk_add_f32 v[100:101], v[100:101], v[82:83] op_sel_hi:[1,0] neg_lo:[0,1] neg_hi:[0,1]
	v_pk_add_f32 v[116:117], v[116:117], v[82:83] op_sel_hi:[1,0] neg_lo:[0,1] neg_hi:[0,1]
	v_pk_add_f32 v[102:103], v[102:103], v[82:83] op_sel_hi:[1,0] neg_lo:[0,1] neg_hi:[0,1]
	v_pk_add_f32 v[118:119], v[118:119], v[82:83] op_sel_hi:[1,0] neg_lo:[0,1] neg_hi:[0,1]
	v_pk_add_f32 v[104:105], v[104:105], v[82:83] op_sel_hi:[1,0] neg_lo:[0,1] neg_hi:[0,1]
	v_pk_add_f32 v[120:121], v[120:121], v[82:83] op_sel_hi:[1,0] neg_lo:[0,1] neg_hi:[0,1]
	v_pk_add_f32 v[106:107], v[106:107], v[82:83] op_sel_hi:[1,0] neg_lo:[0,1] neg_hi:[0,1]
	v_pk_add_f32 v[122:123], v[122:123], v[82:83] op_sel_hi:[1,0] neg_lo:[0,1] neg_hi:[0,1]
	v_pk_add_f32 v[108:109], v[108:109], v[82:83] op_sel_hi:[1,0] neg_lo:[0,1] neg_hi:[0,1]
	v_pk_add_f32 v[124:125], v[124:125], v[82:83] op_sel_hi:[1,0] neg_lo:[0,1] neg_hi:[0,1]
	v_pk_add_f32 v[110:111], v[110:111], v[82:83] op_sel_hi:[1,0] neg_lo:[0,1] neg_hi:[0,1]
	v_pk_add_f32 v[126:127], v[126:127], v[82:83] op_sel_hi:[1,0] neg_lo:[0,1] neg_hi:[0,1]
	v_mov_b32_e32 v81, v80
	v_mov_b32_e32 v82, v80
	v_mov_b32_e32 v83, v80
	v_mov_b32_e32 v84, v80
	v_mov_b32_e32 v85, v80
	v_mov_b32_e32 v86, v80
	v_mov_b32_e32 v87, v80
	v_mov_b32_e32 v88, v80
	v_mov_b32_e32 v89, v80
	v_mov_b32_e32 v90, v80
	v_mov_b32_e32 v91, v80
	v_mov_b32_e32 v92, v80
	v_mov_b32_e32 v93, v80
	v_mov_b32_e32 v94, v80
	v_mov_b32_e32 v95, v80
	s_waitcnt lgkmcnt(0)
	v_pk_mul_f32 v[64:65], v[64:65], v[228:229]
	v_pk_mul_f32 v[66:67], v[66:67], v[230:231]
	v_pk_mul_f32 v[68:69], v[68:69], v[244:245]
	v_pk_mul_f32 v[70:71], v[70:71], v[246:247]
	v_pk_mul_f32 v[72:73], v[72:73], v[248:249]
	v_pk_mul_f32 v[74:75], v[74:75], v[206:207]
	v_pk_mul_f32 v[76:77], v[76:77], v[252:253]
	v_pk_mul_f32 v[78:79], v[78:79], v[202:203]
	v_pk_mul_f32 v[48:49], v[48:49], v[228:229]
	v_pk_mul_f32 v[50:51], v[50:51], v[230:231]
	v_pk_mul_f32 v[52:53], v[52:53], v[244:245]
	v_pk_mul_f32 v[54:55], v[54:55], v[246:247]
	v_pk_mul_f32 v[56:57], v[56:57], v[248:249]
	v_pk_mul_f32 v[58:59], v[58:59], v[206:207]
	v_pk_mul_f32 v[60:61], v[60:61], v[252:253]
	v_pk_mul_f32 v[62:63], v[62:63], v[202:203]
	v_pk_mul_f32 v[32:33], v[32:33], v[228:229]
	v_pk_mul_f32 v[34:35], v[34:35], v[230:231]
	v_pk_mul_f32 v[36:37], v[36:37], v[244:245]
	v_pk_mul_f32 v[38:39], v[38:39], v[246:247]
	v_pk_mul_f32 v[40:41], v[40:41], v[248:249]
	v_pk_mul_f32 v[42:43], v[42:43], v[206:207]
	v_pk_mul_f32 v[44:45], v[44:45], v[252:253]
	v_pk_mul_f32 v[46:47], v[46:47], v[202:203]
	v_pk_mul_f32 v[16:17], v[16:17], v[228:229]
	v_pk_mul_f32 v[18:19], v[18:19], v[230:231]
	v_pk_mul_f32 v[20:21], v[20:21], v[244:245]
	v_pk_mul_f32 v[22:23], v[22:23], v[246:247]
	v_pk_mul_f32 v[24:25], v[24:25], v[248:249]
	v_pk_mul_f32 v[26:27], v[26:27], v[206:207]
	v_pk_mul_f32 v[28:29], v[28:29], v[252:253]
	v_pk_mul_f32 v[30:31], v[30:31], v[202:203]
	v_pk_mul_f32 v[0:1], v[0:1], v[228:229]
	v_pk_mul_f32 v[2:3], v[2:3], v[230:231]
	v_pk_mul_f32 v[4:5], v[4:5], v[244:245]
	v_pk_mul_f32 v[6:7], v[6:7], v[246:247]
	v_pk_mul_f32 v[8:9], v[8:9], v[248:249]
	v_pk_mul_f32 v[10:11], v[10:11], v[206:207]
	v_pk_mul_f32 v[12:13], v[12:13], v[252:253]
	v_pk_mul_f32 v[14:15], v[14:15], v[202:203]
	v_exp_f32_e32 v96, v96
	v_exp_f32_e32 v112, v112
	v_exp_f32_e32 v97, v97
	v_exp_f32_e32 v113, v113
	v_exp_f32_e32 v100, v100
	v_exp_f32_e32 v116, v116
	v_exp_f32_e32 v101, v101
	v_exp_f32_e32 v117, v117
	v_exp_f32_e32 v104, v104
	v_exp_f32_e32 v120, v120
	v_exp_f32_e32 v105, v105
	v_exp_f32_e32 v121, v121
	v_exp_f32_e32 v108, v108
	v_exp_f32_e32 v124, v124
	v_exp_f32_e32 v109, v109
	v_exp_f32_e32 v125, v125
	v_exp_f32_e32 v98, v98
	v_exp_f32_e32 v114, v114
	v_exp_f32_e32 v99, v99
	v_exp_f32_e32 v115, v115
	v_exp_f32_e32 v102, v102
	v_exp_f32_e32 v118, v118
	v_exp_f32_e32 v103, v103
	v_exp_f32_e32 v119, v119
	s_branch .Lfd0_3_join
.Lfd0_0_rare:
	v_mfma_scale_f32_32x32x64_f8f6f4 v[48:63], v[236:243], v[168:175], v[48:63], v219, v219 op_sel_hi:[0,0,0]
	ds_read_b128 v[176:179], v232 offset:40960
	ds_read_b128 v[180:183], v233 offset:40960
	v_mfma_scale_f32_32x32x64_f8f6f4 v[32:47], v[236:243], v[192:199], v[32:47], v219, v219 op_sel_hi:[0,0,0]
	ds_read_b128 v[168:171], v232 offset:43008
	ds_read_b128 v[172:175], v233 offset:43008
	v_mfma_scale_f32_32x32x64_f8f6f4 v[16:31], v[236:243], v[184:191], v[16:31], v219, v219 op_sel_hi:[0,0,0]
	ds_read_b128 v[192:195], v232 offset:45056
	ds_read_b128 v[196:199], v233 offset:45056
	s_nop 15
	s_nop 15
	s_nop 15
	s_nop 15
	s_nop 15
	ds_read_b128 v[184:187], v232 offset:47104
	ds_read_b128 v[188:191], v233 offset:47104
	v_mov_b32_e32 v227, v226
	s_nop 1
	v_permlane32_swap_b32_e32 v226, v227
	v_max3_f32 v226, v226, v227, v227
	s_nop 0
	v_max_f32_e32 v80, v226, v226
	v_max_f32_e32 v82, 0, v80
	s_and_saveexec_b64 s[0:1], s[6:7]
	v_exp_f32_e64 v80, -v82
	s_nop 0
	ds_write_b32 v223, v80 offset:49152
	s_or_b64 exec, exec, s[0:1]
	v_add_u32_e32 v210, s78, v224
	s_waitcnt lgkmcnt(0)
	v_add_u32_e32 v251, 0xc000, v210
	ds_read2_b32 v[228:229], v251 offset1:1
	v_add_u32_e32 v251, 0xc008, v210
	ds_read2_b32 v[230:231], v251 offset1:1
	v_add_u32_e32 v251, 0xc020, v210
	ds_read2_b32 v[244:245], v251 offset1:1
	v_add_u32_e32 v251, 0xc028, v210
	ds_read2_b32 v[246:247], v251 offset1:1
	v_add_u32_e32 v251, 0xc040, v210
	ds_read2_b32 v[248:249], v251 offset1:1
	v_add_u32_e32 v251, 0xc048, v210
	ds_read2_b32 v[206:207], v251 offset1:1
	v_add_u32_e32 v251, 0xc060, v210
	ds_read2_b32 v[252:253], v251 offset1:1
	v_add_u32_e32 v251, 0xc068, v210
	ds_read2_b32 v[202:203], v251 offset1:1
	v_add_f32_e32 v225, v225, v82
	v_xor_b32_e32 v80, 0x80000000, v225
	v_pk_add_f32 v[96:97], v[96:97], v[82:83] op_sel_hi:[1,0] neg_lo:[0,1] neg_hi:[0,1]
	v_pk_add_f32 v[112:113], v[112:113], v[82:83] op_sel_hi:[1,0] neg_lo:[0,1] neg_hi:[0,1]
	v_pk_add_f32 v[98:99], v[98:99], v[82:83] op_sel_hi:[1,0] neg_lo:[0,1] neg_hi:[0,1]
	v_pk_add_f32 v[114:115], v[114:115], v[82:83] op_sel_hi:[1,0] neg_lo:[0,1] neg_hi:[0,1]
	v_pk_add_f32 v[100:101], v[100:101], v[82:83] op_sel_hi:[1,0] neg_lo:[0,1] neg_hi:[0,1]
	v_pk_add_f32 v[116:117], v[116:117], v[82:83] op_sel_hi:[1,0] neg_lo:[0,1] neg_hi:[0,1]
	v_pk_add_f32 v[102:103], v[102:103], v[82:83] op_sel_hi:[1,0] neg_lo:[0,1] neg_hi:[0,1]
	v_pk_add_f32 v[118:119], v[118:119], v[82:83] op_sel_hi:[1,0] neg_lo:[0,1] neg_hi:[0,1]
	v_pk_add_f32 v[104:105], v[104:105], v[82:83] op_sel_hi:[1,0] neg_lo:[0,1] neg_hi:[0,1]
	v_pk_add_f32 v[120:121], v[120:121], v[82:83] op_sel_hi:[1,0] neg_lo:[0,1] neg_hi:[0,1]
	v_pk_add_f32 v[106:107], v[106:107], v[82:83] op_sel_hi:[1,0] neg_lo:[0,1] neg_hi:[0,1]
	v_pk_add_f32 v[122:123], v[122:123], v[82:83] op_sel_hi:[1,0] neg_lo:[0,1] neg_hi:[0,1]
	v_pk_add_f32 v[108:109], v[108:109], v[82:83] op_sel_hi:[1,0] neg_lo:[0,1] neg_hi:[0,1]
	v_pk_add_f32 v[124:125], v[124:125], v[82:83] op_sel_hi:[1,0] neg_lo:[0,1] neg_hi:[0,1]
	v_pk_add_f32 v[110:111], v[110:111], v[82:83] op_sel_hi:[1,0] neg_lo:[0,1] neg_hi:[0,1]
	v_pk_add_f32 v[126:127], v[126:127], v[82:83] op_sel_hi:[1,0] neg_lo:[0,1] neg_hi:[0,1]
	v_mov_b32_e32 v81, v80
	v_mov_b32_e32 v82, v80
	v_mov_b32_e32 v83, v80
	v_mov_b32_e32 v84, v80
	v_mov_b32_e32 v85, v80
	v_mov_b32_e32 v86, v80
	v_mov_b32_e32 v87, v80
	v_mov_b32_e32 v88, v80
	v_mov_b32_e32 v89, v80
	v_mov_b32_e32 v90, v80
	v_mov_b32_e32 v91, v80
	v_mov_b32_e32 v92, v80
	v_mov_b32_e32 v93, v80
	v_mov_b32_e32 v94, v80
	v_mov_b32_e32 v95, v80
	s_waitcnt lgkmcnt(0)
	v_pk_mul_f32 v[64:65], v[64:65], v[228:229]
	v_pk_mul_f32 v[66:67], v[66:67], v[230:231]
	v_pk_mul_f32 v[68:69], v[68:69], v[244:245]
	v_pk_mul_f32 v[70:71], v[70:71], v[246:247]
	v_pk_mul_f32 v[72:73], v[72:73], v[248:249]
	v_pk_mul_f32 v[74:75], v[74:75], v[206:207]
	v_pk_mul_f32 v[76:77], v[76:77], v[252:253]
	v_pk_mul_f32 v[78:79], v[78:79], v[202:203]
	v_pk_mul_f32 v[48:49], v[48:49], v[228:229]
	v_pk_mul_f32 v[50:51], v[50:51], v[230:231]
	v_pk_mul_f32 v[52:53], v[52:53], v[244:245]
	v_pk_mul_f32 v[54:55], v[54:55], v[246:247]
	v_pk_mul_f32 v[56:57], v[56:57], v[248:249]
	v_pk_mul_f32 v[58:59], v[58:59], v[206:207]
	v_pk_mul_f32 v[60:61], v[60:61], v[252:253]
	v_pk_mul_f32 v[62:63], v[62:63], v[202:203]
	v_pk_mul_f32 v[32:33], v[32:33], v[228:229]
	v_pk_mul_f32 v[34:35], v[34:35], v[230:231]
	v_pk_mul_f32 v[36:37], v[36:37], v[244:245]
	v_pk_mul_f32 v[38:39], v[38:39], v[246:247]
	v_pk_mul_f32 v[40:41], v[40:41], v[248:249]
	v_pk_mul_f32 v[42:43], v[42:43], v[206:207]
	v_pk_mul_f32 v[44:45], v[44:45], v[252:253]
	v_pk_mul_f32 v[46:47], v[46:47], v[202:203]
	v_pk_mul_f32 v[16:17], v[16:17], v[228:229]
	v_pk_mul_f32 v[18:19], v[18:19], v[230:231]
	v_pk_mul_f32 v[20:21], v[20:21], v[244:245]
	v_pk_mul_f32 v[22:23], v[22:23], v[246:247]
	v_pk_mul_f32 v[24:25], v[24:25], v[248:249]
	v_pk_mul_f32 v[26:27], v[26:27], v[206:207]
	v_pk_mul_f32 v[28:29], v[28:29], v[252:253]
	v_pk_mul_f32 v[30:31], v[30:31], v[202:203]
	v_pk_mul_f32 v[0:1], v[0:1], v[228:229]
	v_pk_mul_f32 v[2:3], v[2:3], v[230:231]
	v_pk_mul_f32 v[4:5], v[4:5], v[244:245]
	v_pk_mul_f32 v[6:7], v[6:7], v[246:247]
	v_pk_mul_f32 v[8:9], v[8:9], v[248:249]
	v_pk_mul_f32 v[10:11], v[10:11], v[206:207]
	v_pk_mul_f32 v[12:13], v[12:13], v[252:253]
	v_pk_mul_f32 v[14:15], v[14:15], v[202:203]
	v_exp_f32_e32 v96, v96
	v_exp_f32_e32 v112, v112
	v_exp_f32_e32 v97, v97
	v_exp_f32_e32 v113, v113
	v_exp_f32_e32 v100, v100
	v_exp_f32_e32 v116, v116
	v_exp_f32_e32 v101, v101
	v_exp_f32_e32 v117, v117
	v_exp_f32_e32 v104, v104
	v_exp_f32_e32 v120, v120
	v_exp_f32_e32 v105, v105
	v_exp_f32_e32 v121, v121
	v_exp_f32_e32 v108, v108
	v_exp_f32_e32 v124, v124
	v_exp_f32_e32 v109, v109
	v_exp_f32_e32 v125, v125
	v_exp_f32_e32 v98, v98
	v_exp_f32_e32 v114, v114
	v_exp_f32_e32 v99, v99
	v_exp_f32_e32 v115, v115
	v_exp_f32_e32 v102, v102
	v_exp_f32_e32 v118, v118
	v_exp_f32_e32 v103, v103
	v_exp_f32_e32 v119, v119
	s_branch .Lfd0_0_join
.Lfd0_1_rare:
	v_mfma_scale_f32_32x32x64_f8f6f4 v[48:63], v[160:167], v[168:175], v[48:63], v219, v219 op_sel_hi:[0,0,0]
	ds_read_b128 v[176:179], v232 offset:16384
	ds_read_b128 v[180:183], v233 offset:16384
	v_mfma_scale_f32_32x32x64_f8f6f4 v[32:47], v[160:167], v[192:199], v[32:47], v219, v219 op_sel_hi:[0,0,0]
	ds_read_b128 v[168:171], v232 offset:18432
	ds_read_b128 v[172:175], v233 offset:18432
	v_mfma_scale_f32_32x32x64_f8f6f4 v[16:31], v[160:167], v[184:191], v[16:31], v219, v219 op_sel_hi:[0,0,0]
	ds_read_b128 v[192:195], v232 offset:20480
	ds_read_b128 v[196:199], v233 offset:20480
	s_nop 15
	s_nop 15
	s_nop 15
	s_nop 15
	s_nop 15
	ds_read_b128 v[184:187], v232 offset:22528
	ds_read_b128 v[188:191], v233 offset:22528
	v_mov_b32_e32 v227, v226
	s_nop 1
	v_permlane32_swap_b32_e32 v226, v227
	v_max3_f32 v226, v226, v227, v227
	s_nop 0
	v_max_f32_e32 v80, v226, v226
	v_max_f32_e32 v82, 0, v80
	s_and_saveexec_b64 s[0:1], s[6:7]
	v_exp_f32_e64 v80, -v82
	s_nop 0
	ds_write_b32 v223, v80 offset:49152
	s_or_b64 exec, exec, s[0:1]
	v_add_u32_e32 v210, s78, v224
	s_waitcnt lgkmcnt(0)
	v_add_u32_e32 v251, 0xc000, v210
	ds_read2_b32 v[228:229], v251 offset1:1
	v_add_u32_e32 v251, 0xc008, v210
	ds_read2_b32 v[230:231], v251 offset1:1
	v_add_u32_e32 v251, 0xc020, v210
	ds_read2_b32 v[244:245], v251 offset1:1
	v_add_u32_e32 v251, 0xc028, v210
	ds_read2_b32 v[246:247], v251 offset1:1
	v_add_u32_e32 v251, 0xc040, v210
	ds_read2_b32 v[248:249], v251 offset1:1
	v_add_u32_e32 v251, 0xc048, v210
	ds_read2_b32 v[206:207], v251 offset1:1
	v_add_u32_e32 v251, 0xc060, v210
	ds_read2_b32 v[252:253], v251 offset1:1
	v_add_u32_e32 v251, 0xc068, v210
	ds_read2_b32 v[202:203], v251 offset1:1
	v_add_f32_e32 v225, v225, v82
	v_xor_b32_e32 v80, 0x80000000, v225
	v_pk_add_f32 v[96:97], v[96:97], v[82:83] op_sel_hi:[1,0] neg_lo:[0,1] neg_hi:[0,1]
	v_pk_add_f32 v[112:113], v[112:113], v[82:83] op_sel_hi:[1,0] neg_lo:[0,1] neg_hi:[0,1]
	v_pk_add_f32 v[98:99], v[98:99], v[82:83] op_sel_hi:[1,0] neg_lo:[0,1] neg_hi:[0,1]
	v_pk_add_f32 v[114:115], v[114:115], v[82:83] op_sel_hi:[1,0] neg_lo:[0,1] neg_hi:[0,1]
	v_pk_add_f32 v[100:101], v[100:101], v[82:83] op_sel_hi:[1,0] neg_lo:[0,1] neg_hi:[0,1]
	v_pk_add_f32 v[116:117], v[116:117], v[82:83] op_sel_hi:[1,0] neg_lo:[0,1] neg_hi:[0,1]
	v_pk_add_f32 v[102:103], v[102:103], v[82:83] op_sel_hi:[1,0] neg_lo:[0,1] neg_hi:[0,1]
	v_pk_add_f32 v[118:119], v[118:119], v[82:83] op_sel_hi:[1,0] neg_lo:[0,1] neg_hi:[0,1]
	v_pk_add_f32 v[104:105], v[104:105], v[82:83] op_sel_hi:[1,0] neg_lo:[0,1] neg_hi:[0,1]
	v_pk_add_f32 v[120:121], v[120:121], v[82:83] op_sel_hi:[1,0] neg_lo:[0,1] neg_hi:[0,1]
	v_pk_add_f32 v[106:107], v[106:107], v[82:83] op_sel_hi:[1,0] neg_lo:[0,1] neg_hi:[0,1]
	v_pk_add_f32 v[122:123], v[122:123], v[82:83] op_sel_hi:[1,0] neg_lo:[0,1] neg_hi:[0,1]
	v_pk_add_f32 v[108:109], v[108:109], v[82:83] op_sel_hi:[1,0] neg_lo:[0,1] neg_hi:[0,1]
	v_pk_add_f32 v[124:125], v[124:125], v[82:83] op_sel_hi:[1,0] neg_lo:[0,1] neg_hi:[0,1]
	v_pk_add_f32 v[110:111], v[110:111], v[82:83] op_sel_hi:[1,0] neg_lo:[0,1] neg_hi:[0,1]
	v_pk_add_f32 v[126:127], v[126:127], v[82:83] op_sel_hi:[1,0] neg_lo:[0,1] neg_hi:[0,1]
	v_mov_b32_e32 v81, v80
	v_mov_b32_e32 v82, v80
	v_mov_b32_e32 v83, v80
	v_mov_b32_e32 v84, v80
	v_mov_b32_e32 v85, v80
	v_mov_b32_e32 v86, v80
	v_mov_b32_e32 v87, v80
	v_mov_b32_e32 v88, v80
	v_mov_b32_e32 v89, v80
	v_mov_b32_e32 v90, v80
	v_mov_b32_e32 v91, v80
	v_mov_b32_e32 v92, v80
	v_mov_b32_e32 v93, v80
	v_mov_b32_e32 v94, v80
	v_mov_b32_e32 v95, v80
	s_waitcnt lgkmcnt(0)
	v_pk_mul_f32 v[64:65], v[64:65], v[228:229]
	v_pk_mul_f32 v[66:67], v[66:67], v[230:231]
	v_pk_mul_f32 v[68:69], v[68:69], v[244:245]
	v_pk_mul_f32 v[70:71], v[70:71], v[246:247]
	v_pk_mul_f32 v[72:73], v[72:73], v[248:249]
	v_pk_mul_f32 v[74:75], v[74:75], v[206:207]
	v_pk_mul_f32 v[76:77], v[76:77], v[252:253]
	v_pk_mul_f32 v[78:79], v[78:79], v[202:203]
	v_pk_mul_f32 v[48:49], v[48:49], v[228:229]
	v_pk_mul_f32 v[50:51], v[50:51], v[230:231]
	v_pk_mul_f32 v[52:53], v[52:53], v[244:245]
	v_pk_mul_f32 v[54:55], v[54:55], v[246:247]
	v_pk_mul_f32 v[56:57], v[56:57], v[248:249]
	v_pk_mul_f32 v[58:59], v[58:59], v[206:207]
	v_pk_mul_f32 v[60:61], v[60:61], v[252:253]
	v_pk_mul_f32 v[62:63], v[62:63], v[202:203]
	v_pk_mul_f32 v[32:33], v[32:33], v[228:229]
	v_pk_mul_f32 v[34:35], v[34:35], v[230:231]
	v_pk_mul_f32 v[36:37], v[36:37], v[244:245]
	v_pk_mul_f32 v[38:39], v[38:39], v[246:247]
	v_pk_mul_f32 v[40:41], v[40:41], v[248:249]
	v_pk_mul_f32 v[42:43], v[42:43], v[206:207]
	v_pk_mul_f32 v[44:45], v[44:45], v[252:253]
	v_pk_mul_f32 v[46:47], v[46:47], v[202:203]
	v_pk_mul_f32 v[16:17], v[16:17], v[228:229]
	v_pk_mul_f32 v[18:19], v[18:19], v[230:231]
	v_pk_mul_f32 v[20:21], v[20:21], v[244:245]
	v_pk_mul_f32 v[22:23], v[22:23], v[246:247]
	v_pk_mul_f32 v[24:25], v[24:25], v[248:249]
	v_pk_mul_f32 v[26:27], v[26:27], v[206:207]
	v_pk_mul_f32 v[28:29], v[28:29], v[252:253]
	v_pk_mul_f32 v[30:31], v[30:31], v[202:203]
	v_pk_mul_f32 v[0:1], v[0:1], v[228:229]
	v_pk_mul_f32 v[2:3], v[2:3], v[230:231]
	v_pk_mul_f32 v[4:5], v[4:5], v[244:245]
	v_pk_mul_f32 v[6:7], v[6:7], v[246:247]
	v_pk_mul_f32 v[8:9], v[8:9], v[248:249]
	v_pk_mul_f32 v[10:11], v[10:11], v[206:207]
	v_pk_mul_f32 v[12:13], v[12:13], v[252:253]
	v_pk_mul_f32 v[14:15], v[14:15], v[202:203]
	v_exp_f32_e32 v96, v96
	v_exp_f32_e32 v112, v112
	v_exp_f32_e32 v97, v97
	v_exp_f32_e32 v113, v113
	v_exp_f32_e32 v100, v100
	v_exp_f32_e32 v116, v116
	v_exp_f32_e32 v101, v101
	v_exp_f32_e32 v117, v117
	v_exp_f32_e32 v104, v104
	v_exp_f32_e32 v120, v120
	v_exp_f32_e32 v105, v105
	v_exp_f32_e32 v121, v121
	v_exp_f32_e32 v108, v108
	v_exp_f32_e32 v124, v124
	v_exp_f32_e32 v109, v109
	v_exp_f32_e32 v125, v125
	v_exp_f32_e32 v98, v98
	v_exp_f32_e32 v114, v114
	v_exp_f32_e32 v99, v99
	v_exp_f32_e32 v115, v115
	v_exp_f32_e32 v102, v102
	v_exp_f32_e32 v118, v118
	v_exp_f32_e32 v103, v103
	v_exp_f32_e32 v119, v119
	s_branch .Lfd0_1_join
.Lfd0_2_rare:
	v_mfma_scale_f32_32x32x64_f8f6f4 v[48:63], v[236:243], v[168:175], v[48:63], v219, v219 op_sel_hi:[0,0,0]
	ds_read_b128 v[176:179], v232 offset:24576
	ds_read_b128 v[180:183], v233 offset:24576
	v_mfma_scale_f32_32x32x64_f8f6f4 v[32:47], v[236:243], v[192:199], v[32:47], v219, v219 op_sel_hi:[0,0,0]
	ds_read_b128 v[168:171], v232 offset:26624
	ds_read_b128 v[172:175], v233 offset:26624
	v_mfma_scale_f32_32x32x64_f8f6f4 v[16:31], v[236:243], v[184:191], v[16:31], v219, v219 op_sel_hi:[0,0,0]
	ds_read_b128 v[192:195], v232 offset:28672
	ds_read_b128 v[196:199], v233 offset:28672
	s_nop 15
	s_nop 15
	s_nop 15
	s_nop 15
	s_nop 15
	ds_read_b128 v[184:187], v232 offset:30720
	ds_read_b128 v[188:191], v233 offset:30720
	v_mov_b32_e32 v227, v226
	s_nop 1
	v_permlane32_swap_b32_e32 v226, v227
	v_max3_f32 v226, v226, v227, v227
	s_nop 0
	v_max_f32_e32 v80, v226, v226
	v_max_f32_e32 v82, 0, v80
	s_and_saveexec_b64 s[0:1], s[6:7]
	v_exp_f32_e64 v80, -v82
	s_nop 0
	ds_write_b32 v223, v80 offset:49152
	s_or_b64 exec, exec, s[0:1]
	v_add_u32_e32 v210, s78, v224
	s_waitcnt lgkmcnt(0)
	v_add_u32_e32 v251, 0xc000, v210
	ds_read2_b32 v[228:229], v251 offset1:1
	v_add_u32_e32 v251, 0xc008, v210
	ds_read2_b32 v[230:231], v251 offset1:1
	v_add_u32_e32 v251, 0xc020, v210
	ds_read2_b32 v[244:245], v251 offset1:1
	v_add_u32_e32 v251, 0xc028, v210
	ds_read2_b32 v[246:247], v251 offset1:1
	v_add_u32_e32 v251, 0xc040, v210
	ds_read2_b32 v[248:249], v251 offset1:1
	v_add_u32_e32 v251, 0xc048, v210
	ds_read2_b32 v[206:207], v251 offset1:1
	v_add_u32_e32 v251, 0xc060, v210
	ds_read2_b32 v[252:253], v251 offset1:1
	v_add_u32_e32 v251, 0xc068, v210
	ds_read2_b32 v[202:203], v251 offset1:1
	v_add_f32_e32 v225, v225, v82
	v_xor_b32_e32 v80, 0x80000000, v225
	v_pk_add_f32 v[96:97], v[96:97], v[82:83] op_sel_hi:[1,0] neg_lo:[0,1] neg_hi:[0,1]
	v_pk_add_f32 v[112:113], v[112:113], v[82:83] op_sel_hi:[1,0] neg_lo:[0,1] neg_hi:[0,1]
	v_pk_add_f32 v[98:99], v[98:99], v[82:83] op_sel_hi:[1,0] neg_lo:[0,1] neg_hi:[0,1]
	v_pk_add_f32 v[114:115], v[114:115], v[82:83] op_sel_hi:[1,0] neg_lo:[0,1] neg_hi:[0,1]
	v_pk_add_f32 v[100:101], v[100:101], v[82:83] op_sel_hi:[1,0] neg_lo:[0,1] neg_hi:[0,1]
	v_pk_add_f32 v[116:117], v[116:117], v[82:83] op_sel_hi:[1,0] neg_lo:[0,1] neg_hi:[0,1]
	v_pk_add_f32 v[102:103], v[102:103], v[82:83] op_sel_hi:[1,0] neg_lo:[0,1] neg_hi:[0,1]
	v_pk_add_f32 v[118:119], v[118:119], v[82:83] op_sel_hi:[1,0] neg_lo:[0,1] neg_hi:[0,1]
	v_pk_add_f32 v[104:105], v[104:105], v[82:83] op_sel_hi:[1,0] neg_lo:[0,1] neg_hi:[0,1]
	v_pk_add_f32 v[120:121], v[120:121], v[82:83] op_sel_hi:[1,0] neg_lo:[0,1] neg_hi:[0,1]
	v_pk_add_f32 v[106:107], v[106:107], v[82:83] op_sel_hi:[1,0] neg_lo:[0,1] neg_hi:[0,1]
	v_pk_add_f32 v[122:123], v[122:123], v[82:83] op_sel_hi:[1,0] neg_lo:[0,1] neg_hi:[0,1]
	v_pk_add_f32 v[108:109], v[108:109], v[82:83] op_sel_hi:[1,0] neg_lo:[0,1] neg_hi:[0,1]
	v_pk_add_f32 v[124:125], v[124:125], v[82:83] op_sel_hi:[1,0] neg_lo:[0,1] neg_hi:[0,1]
	v_pk_add_f32 v[110:111], v[110:111], v[82:83] op_sel_hi:[1,0] neg_lo:[0,1] neg_hi:[0,1]
	v_pk_add_f32 v[126:127], v[126:127], v[82:83] op_sel_hi:[1,0] neg_lo:[0,1] neg_hi:[0,1]
	v_mov_b32_e32 v81, v80
	v_mov_b32_e32 v82, v80
	v_mov_b32_e32 v83, v80
	v_mov_b32_e32 v84, v80
	v_mov_b32_e32 v85, v80
	v_mov_b32_e32 v86, v80
	v_mov_b32_e32 v87, v80
	v_mov_b32_e32 v88, v80
	v_mov_b32_e32 v89, v80
	v_mov_b32_e32 v90, v80
	v_mov_b32_e32 v91, v80
	v_mov_b32_e32 v92, v80
	v_mov_b32_e32 v93, v80
	v_mov_b32_e32 v94, v80
	v_mov_b32_e32 v95, v80
	s_waitcnt lgkmcnt(0)
	v_pk_mul_f32 v[64:65], v[64:65], v[228:229]
	v_pk_mul_f32 v[66:67], v[66:67], v[230:231]
	v_pk_mul_f32 v[68:69], v[68:69], v[244:245]
	v_pk_mul_f32 v[70:71], v[70:71], v[246:247]
	v_pk_mul_f32 v[72:73], v[72:73], v[248:249]
	v_pk_mul_f32 v[74:75], v[74:75], v[206:207]
	v_pk_mul_f32 v[76:77], v[76:77], v[252:253]
	v_pk_mul_f32 v[78:79], v[78:79], v[202:203]
	v_pk_mul_f32 v[48:49], v[48:49], v[228:229]
	v_pk_mul_f32 v[50:51], v[50:51], v[230:231]
	v_pk_mul_f32 v[52:53], v[52:53], v[244:245]
	v_pk_mul_f32 v[54:55], v[54:55], v[246:247]
	v_pk_mul_f32 v[56:57], v[56:57], v[248:249]
	v_pk_mul_f32 v[58:59], v[58:59], v[206:207]
	v_pk_mul_f32 v[60:61], v[60:61], v[252:253]
	v_pk_mul_f32 v[62:63], v[62:63], v[202:203]
	v_pk_mul_f32 v[32:33], v[32:33], v[228:229]
	v_pk_mul_f32 v[34:35], v[34:35], v[230:231]
	v_pk_mul_f32 v[36:37], v[36:37], v[244:245]
	v_pk_mul_f32 v[38:39], v[38:39], v[246:247]
	v_pk_mul_f32 v[40:41], v[40:41], v[248:249]
	v_pk_mul_f32 v[42:43], v[42:43], v[206:207]
	v_pk_mul_f32 v[44:45], v[44:45], v[252:253]
	v_pk_mul_f32 v[46:47], v[46:47], v[202:203]
	v_pk_mul_f32 v[16:17], v[16:17], v[228:229]
	v_pk_mul_f32 v[18:19], v[18:19], v[230:231]
	v_pk_mul_f32 v[20:21], v[20:21], v[244:245]
	v_pk_mul_f32 v[22:23], v[22:23], v[246:247]
	v_pk_mul_f32 v[24:25], v[24:25], v[248:249]
	v_pk_mul_f32 v[26:27], v[26:27], v[206:207]
	v_pk_mul_f32 v[28:29], v[28:29], v[252:253]
	v_pk_mul_f32 v[30:31], v[30:31], v[202:203]
	v_pk_mul_f32 v[0:1], v[0:1], v[228:229]
	v_pk_mul_f32 v[2:3], v[2:3], v[230:231]
	v_pk_mul_f32 v[4:5], v[4:5], v[244:245]
	v_pk_mul_f32 v[6:7], v[6:7], v[246:247]
	v_pk_mul_f32 v[8:9], v[8:9], v[248:249]
	v_pk_mul_f32 v[10:11], v[10:11], v[206:207]
	v_pk_mul_f32 v[12:13], v[12:13], v[252:253]
	v_pk_mul_f32 v[14:15], v[14:15], v[202:203]
	v_exp_f32_e32 v96, v96
	v_exp_f32_e32 v112, v112
	v_exp_f32_e32 v97, v97
	v_exp_f32_e32 v113, v113
	v_exp_f32_e32 v100, v100
	v_exp_f32_e32 v116, v116
	v_exp_f32_e32 v101, v101
	v_exp_f32_e32 v117, v117
	v_exp_f32_e32 v104, v104
	v_exp_f32_e32 v120, v120
	v_exp_f32_e32 v105, v105
	v_exp_f32_e32 v121, v121
	v_exp_f32_e32 v108, v108
	v_exp_f32_e32 v124, v124
	v_exp_f32_e32 v109, v109
	v_exp_f32_e32 v125, v125
	v_exp_f32_e32 v98, v98
	v_exp_f32_e32 v114, v114
	v_exp_f32_e32 v99, v99
	v_exp_f32_e32 v115, v115
	v_exp_f32_e32 v102, v102
	v_exp_f32_e32 v118, v118
	v_exp_f32_e32 v103, v103
	v_exp_f32_e32 v119, v119
	s_branch .Lfd0_2_join
.Lfd0dA_rare:
	v_mfma_scale_f32_32x32x64_f8f6f4 v[48:63], v[160:167], v[168:175], v[48:63], v219, v219 op_sel_hi:[0,0,0]
	v_mfma_scale_f32_32x32x64_f8f6f4 v[32:47], v[160:167], v[192:199], v[32:47], v219, v219 op_sel_hi:[0,0,0]
	v_mfma_scale_f32_32x32x64_f8f6f4 v[16:31], v[160:167], v[184:191], v[16:31], v219, v219 op_sel_hi:[0,0,0]
	s_nop 15
	s_nop 15
	s_nop 15
	s_nop 15
	s_nop 15
	v_mov_b32_e32 v227, v226
	s_nop 1
	v_permlane32_swap_b32_e32 v226, v227
	v_max3_f32 v226, v226, v227, v227
	s_nop 0
	v_max_f32_e32 v80, v226, v226
	v_max_f32_e32 v82, 0, v80
	s_and_saveexec_b64 s[0:1], s[6:7]
	v_exp_f32_e64 v80, -v82
	s_nop 0
	ds_write_b32 v223, v80 offset:49152
	s_or_b64 exec, exec, s[0:1]
	v_add_u32_e32 v210, s78, v224
	s_waitcnt lgkmcnt(0)
	v_add_u32_e32 v251, 0xc000, v210
	ds_read2_b32 v[228:229], v251 offset1:1
	v_add_u32_e32 v251, 0xc008, v210
	ds_read2_b32 v[230:231], v251 offset1:1
	v_add_u32_e32 v251, 0xc020, v210
	ds_read2_b32 v[244:245], v251 offset1:1
	v_add_u32_e32 v251, 0xc028, v210
	ds_read2_b32 v[246:247], v251 offset1:1
	v_add_u32_e32 v251, 0xc040, v210
	ds_read2_b32 v[248:249], v251 offset1:1
	v_add_u32_e32 v251, 0xc048, v210
	ds_read2_b32 v[206:207], v251 offset1:1
	v_add_u32_e32 v251, 0xc060, v210
	ds_read2_b32 v[252:253], v251 offset1:1
	v_add_u32_e32 v251, 0xc068, v210
	ds_read2_b32 v[202:203], v251 offset1:1
	v_add_f32_e32 v225, v225, v82
	v_xor_b32_e32 v80, 0x80000000, v225
	v_pk_add_f32 v[96:97], v[96:97], v[82:83] op_sel_hi:[1,0] neg_lo:[0,1] neg_hi:[0,1]
	v_pk_add_f32 v[112:113], v[112:113], v[82:83] op_sel_hi:[1,0] neg_lo:[0,1] neg_hi:[0,1]
	v_pk_add_f32 v[98:99], v[98:99], v[82:83] op_sel_hi:[1,0] neg_lo:[0,1] neg_hi:[0,1]
	v_pk_add_f32 v[114:115], v[114:115], v[82:83] op_sel_hi:[1,0] neg_lo:[0,1] neg_hi:[0,1]
	v_pk_add_f32 v[100:101], v[100:101], v[82:83] op_sel_hi:[1,0] neg_lo:[0,1] neg_hi:[0,1]
	v_pk_add_f32 v[116:117], v[116:117], v[82:83] op_sel_hi:[1,0] neg_lo:[0,1] neg_hi:[0,1]
	v_pk_add_f32 v[102:103], v[102:103], v[82:83] op_sel_hi:[1,0] neg_lo:[0,1] neg_hi:[0,1]
	v_pk_add_f32 v[118:119], v[118:119], v[82:83] op_sel_hi:[1,0] neg_lo:[0,1] neg_hi:[0,1]
	v_pk_add_f32 v[104:105], v[104:105], v[82:83] op_sel_hi:[1,0] neg_lo:[0,1] neg_hi:[0,1]
	v_pk_add_f32 v[120:121], v[120:121], v[82:83] op_sel_hi:[1,0] neg_lo:[0,1] neg_hi:[0,1]
	v_pk_add_f32 v[106:107], v[106:107], v[82:83] op_sel_hi:[1,0] neg_lo:[0,1] neg_hi:[0,1]
	v_pk_add_f32 v[122:123], v[122:123], v[82:83] op_sel_hi:[1,0] neg_lo:[0,1] neg_hi:[0,1]
	v_pk_add_f32 v[108:109], v[108:109], v[82:83] op_sel_hi:[1,0] neg_lo:[0,1] neg_hi:[0,1]
	v_pk_add_f32 v[124:125], v[124:125], v[82:83] op_sel_hi:[1,0] neg_lo:[0,1] neg_hi:[0,1]
	v_pk_add_f32 v[110:111], v[110:111], v[82:83] op_sel_hi:[1,0] neg_lo:[0,1] neg_hi:[0,1]
	v_pk_add_f32 v[126:127], v[126:127], v[82:83] op_sel_hi:[1,0] neg_lo:[0,1] neg_hi:[0,1]
	v_mov_b32_e32 v81, v80
	v_mov_b32_e32 v82, v80
	v_mov_b32_e32 v83, v80
	v_mov_b32_e32 v84, v80
	v_mov_b32_e32 v85, v80
	v_mov_b32_e32 v86, v80
	v_mov_b32_e32 v87, v80
	v_mov_b32_e32 v88, v80
	v_mov_b32_e32 v89, v80
	v_mov_b32_e32 v90, v80
	v_mov_b32_e32 v91, v80
	v_mov_b32_e32 v92, v80
	v_mov_b32_e32 v93, v80
	v_mov_b32_e32 v94, v80
	v_mov_b32_e32 v95, v80
	s_waitcnt lgkmcnt(0)
	v_pk_mul_f32 v[64:65], v[64:65], v[228:229]
	v_pk_mul_f32 v[66:67], v[66:67], v[230:231]
	v_pk_mul_f32 v[68:69], v[68:69], v[244:245]
	v_pk_mul_f32 v[70:71], v[70:71], v[246:247]
	v_pk_mul_f32 v[72:73], v[72:73], v[248:249]
	v_pk_mul_f32 v[74:75], v[74:75], v[206:207]
	v_pk_mul_f32 v[76:77], v[76:77], v[252:253]
	v_pk_mul_f32 v[78:79], v[78:79], v[202:203]
	v_pk_mul_f32 v[48:49], v[48:49], v[228:229]
	v_pk_mul_f32 v[50:51], v[50:51], v[230:231]
	v_pk_mul_f32 v[52:53], v[52:53], v[244:245]
	v_pk_mul_f32 v[54:55], v[54:55], v[246:247]
	v_pk_mul_f32 v[56:57], v[56:57], v[248:249]
	v_pk_mul_f32 v[58:59], v[58:59], v[206:207]
	v_pk_mul_f32 v[60:61], v[60:61], v[252:253]
	v_pk_mul_f32 v[62:63], v[62:63], v[202:203]
	v_pk_mul_f32 v[32:33], v[32:33], v[228:229]
	v_pk_mul_f32 v[34:35], v[34:35], v[230:231]
	v_pk_mul_f32 v[36:37], v[36:37], v[244:245]
	v_pk_mul_f32 v[38:39], v[38:39], v[246:247]
	v_pk_mul_f32 v[40:41], v[40:41], v[248:249]
	v_pk_mul_f32 v[42:43], v[42:43], v[206:207]
	v_pk_mul_f32 v[44:45], v[44:45], v[252:253]
	v_pk_mul_f32 v[46:47], v[46:47], v[202:203]
	v_pk_mul_f32 v[16:17], v[16:17], v[228:229]
	v_pk_mul_f32 v[18:19], v[18:19], v[230:231]
	v_pk_mul_f32 v[20:21], v[20:21], v[244:245]
	v_pk_mul_f32 v[22:23], v[22:23], v[246:247]
	v_pk_mul_f32 v[24:25], v[24:25], v[248:249]
	v_pk_mul_f32 v[26:27], v[26:27], v[206:207]
	v_pk_mul_f32 v[28:29], v[28:29], v[252:253]
	v_pk_mul_f32 v[30:31], v[30:31], v[202:203]
	v_pk_mul_f32 v[0:1], v[0:1], v[228:229]
	v_pk_mul_f32 v[2:3], v[2:3], v[230:231]
	v_pk_mul_f32 v[4:5], v[4:5], v[244:245]
	v_pk_mul_f32 v[6:7], v[6:7], v[246:247]
	v_pk_mul_f32 v[8:9], v[8:9], v[248:249]
	v_pk_mul_f32 v[10:11], v[10:11], v[206:207]
	v_pk_mul_f32 v[12:13], v[12:13], v[252:253]
	v_pk_mul_f32 v[14:15], v[14:15], v[202:203]
	v_exp_f32_e32 v96, v96
	v_exp_f32_e32 v112, v112
	v_exp_f32_e32 v97, v97
	v_exp_f32_e32 v113, v113
	v_exp_f32_e32 v100, v100
	v_exp_f32_e32 v116, v116
	v_exp_f32_e32 v101, v101
	v_exp_f32_e32 v117, v117
	v_exp_f32_e32 v104, v104
	v_exp_f32_e32 v120, v120
	v_exp_f32_e32 v105, v105
	v_exp_f32_e32 v121, v121
	v_exp_f32_e32 v108, v108
	v_exp_f32_e32 v124, v124
	v_exp_f32_e32 v109, v109
	v_exp_f32_e32 v125, v125
	v_exp_f32_e32 v98, v98
	v_exp_f32_e32 v114, v114
	v_exp_f32_e32 v99, v99
	v_exp_f32_e32 v115, v115
	v_exp_f32_e32 v102, v102
	v_exp_f32_e32 v118, v118
	v_exp_f32_e32 v103, v103
	v_exp_f32_e32 v119, v119
	s_branch .Lfd0dA_join
.Lfd0dB_rare:
	v_mfma_scale_f32_32x32x64_f8f6f4 v[48:63], v[236:243], v[168:175], v[48:63], v219, v219 op_sel_hi:[0,0,0]
	v_mfma_scale_f32_32x32x64_f8f6f4 v[32:47], v[236:243], v[192:199], v[32:47], v219, v219 op_sel_hi:[0,0,0]
	v_mfma_scale_f32_32x32x64_f8f6f4 v[16:31], v[236:243], v[184:191], v[16:31], v219, v219 op_sel_hi:[0,0,0]
	s_nop 15
	s_nop 15
	s_nop 15
	s_nop 15
	s_nop 15
	v_mov_b32_e32 v227, v226
	s_nop 1
	v_permlane32_swap_b32_e32 v226, v227
	v_max3_f32 v226, v226, v227, v227
	s_nop 0
	v_max_f32_e32 v80, v226, v226
	v_max_f32_e32 v82, 0, v80
	s_and_saveexec_b64 s[0:1], s[6:7]
	v_exp_f32_e64 v80, -v82
	s_nop 0
	ds_write_b32 v223, v80 offset:49152
	s_or_b64 exec, exec, s[0:1]
	v_add_u32_e32 v210, s78, v224
	s_waitcnt lgkmcnt(0)
	v_add_u32_e32 v251, 0xc000, v210
	ds_read2_b32 v[228:229], v251 offset1:1
	v_add_u32_e32 v251, 0xc008, v210
	ds_read2_b32 v[230:231], v251 offset1:1
	v_add_u32_e32 v251, 0xc020, v210
	ds_read2_b32 v[244:245], v251 offset1:1
	v_add_u32_e32 v251, 0xc028, v210
	ds_read2_b32 v[246:247], v251 offset1:1
	v_add_u32_e32 v251, 0xc040, v210
	ds_read2_b32 v[248:249], v251 offset1:1
	v_add_u32_e32 v251, 0xc048, v210
	ds_read2_b32 v[206:207], v251 offset1:1
	v_add_u32_e32 v251, 0xc060, v210
	ds_read2_b32 v[252:253], v251 offset1:1
	v_add_u32_e32 v251, 0xc068, v210
	ds_read2_b32 v[202:203], v251 offset1:1
	v_add_f32_e32 v225, v225, v82
	v_xor_b32_e32 v80, 0x80000000, v225
	v_pk_add_f32 v[96:97], v[96:97], v[82:83] op_sel_hi:[1,0] neg_lo:[0,1] neg_hi:[0,1]
	v_pk_add_f32 v[112:113], v[112:113], v[82:83] op_sel_hi:[1,0] neg_lo:[0,1] neg_hi:[0,1]
	v_pk_add_f32 v[98:99], v[98:99], v[82:83] op_sel_hi:[1,0] neg_lo:[0,1] neg_hi:[0,1]
	v_pk_add_f32 v[114:115], v[114:115], v[82:83] op_sel_hi:[1,0] neg_lo:[0,1] neg_hi:[0,1]
	v_pk_add_f32 v[100:101], v[100:101], v[82:83] op_sel_hi:[1,0] neg_lo:[0,1] neg_hi:[0,1]
	v_pk_add_f32 v[116:117], v[116:117], v[82:83] op_sel_hi:[1,0] neg_lo:[0,1] neg_hi:[0,1]
	v_pk_add_f32 v[102:103], v[102:103], v[82:83] op_sel_hi:[1,0] neg_lo:[0,1] neg_hi:[0,1]
	v_pk_add_f32 v[118:119], v[118:119], v[82:83] op_sel_hi:[1,0] neg_lo:[0,1] neg_hi:[0,1]
	v_pk_add_f32 v[104:105], v[104:105], v[82:83] op_sel_hi:[1,0] neg_lo:[0,1] neg_hi:[0,1]
	v_pk_add_f32 v[120:121], v[120:121], v[82:83] op_sel_hi:[1,0] neg_lo:[0,1] neg_hi:[0,1]
	v_pk_add_f32 v[106:107], v[106:107], v[82:83] op_sel_hi:[1,0] neg_lo:[0,1] neg_hi:[0,1]
	v_pk_add_f32 v[122:123], v[122:123], v[82:83] op_sel_hi:[1,0] neg_lo:[0,1] neg_hi:[0,1]
	v_pk_add_f32 v[108:109], v[108:109], v[82:83] op_sel_hi:[1,0] neg_lo:[0,1] neg_hi:[0,1]
	v_pk_add_f32 v[124:125], v[124:125], v[82:83] op_sel_hi:[1,0] neg_lo:[0,1] neg_hi:[0,1]
	v_pk_add_f32 v[110:111], v[110:111], v[82:83] op_sel_hi:[1,0] neg_lo:[0,1] neg_hi:[0,1]
	v_pk_add_f32 v[126:127], v[126:127], v[82:83] op_sel_hi:[1,0] neg_lo:[0,1] neg_hi:[0,1]
	v_mov_b32_e32 v81, v80
	v_mov_b32_e32 v82, v80
	v_mov_b32_e32 v83, v80
	v_mov_b32_e32 v84, v80
	v_mov_b32_e32 v85, v80
	v_mov_b32_e32 v86, v80
	v_mov_b32_e32 v87, v80
	v_mov_b32_e32 v88, v80
	v_mov_b32_e32 v89, v80
	v_mov_b32_e32 v90, v80
	v_mov_b32_e32 v91, v80
	v_mov_b32_e32 v92, v80
	v_mov_b32_e32 v93, v80
	v_mov_b32_e32 v94, v80
	v_mov_b32_e32 v95, v80
	s_waitcnt lgkmcnt(0)
	v_pk_mul_f32 v[64:65], v[64:65], v[228:229]
	v_pk_mul_f32 v[66:67], v[66:67], v[230:231]
	v_pk_mul_f32 v[68:69], v[68:69], v[244:245]
	v_pk_mul_f32 v[70:71], v[70:71], v[246:247]
	v_pk_mul_f32 v[72:73], v[72:73], v[248:249]
	v_pk_mul_f32 v[74:75], v[74:75], v[206:207]
	v_pk_mul_f32 v[76:77], v[76:77], v[252:253]
	v_pk_mul_f32 v[78:79], v[78:79], v[202:203]
	v_pk_mul_f32 v[48:49], v[48:49], v[228:229]
	v_pk_mul_f32 v[50:51], v[50:51], v[230:231]
	v_pk_mul_f32 v[52:53], v[52:53], v[244:245]
	v_pk_mul_f32 v[54:55], v[54:55], v[246:247]
	v_pk_mul_f32 v[56:57], v[56:57], v[248:249]
	v_pk_mul_f32 v[58:59], v[58:59], v[206:207]
	v_pk_mul_f32 v[60:61], v[60:61], v[252:253]
	v_pk_mul_f32 v[62:63], v[62:63], v[202:203]
	v_pk_mul_f32 v[32:33], v[32:33], v[228:229]
	v_pk_mul_f32 v[34:35], v[34:35], v[230:231]
	v_pk_mul_f32 v[36:37], v[36:37], v[244:245]
	v_pk_mul_f32 v[38:39], v[38:39], v[246:247]
	v_pk_mul_f32 v[40:41], v[40:41], v[248:249]
	v_pk_mul_f32 v[42:43], v[42:43], v[206:207]
	v_pk_mul_f32 v[44:45], v[44:45], v[252:253]
	v_pk_mul_f32 v[46:47], v[46:47], v[202:203]
	v_pk_mul_f32 v[16:17], v[16:17], v[228:229]
	v_pk_mul_f32 v[18:19], v[18:19], v[230:231]
	v_pk_mul_f32 v[20:21], v[20:21], v[244:245]
	v_pk_mul_f32 v[22:23], v[22:23], v[246:247]
	v_pk_mul_f32 v[24:25], v[24:25], v[248:249]
	v_pk_mul_f32 v[26:27], v[26:27], v[206:207]
	v_pk_mul_f32 v[28:29], v[28:29], v[252:253]
	v_pk_mul_f32 v[30:31], v[30:31], v[202:203]
	v_pk_mul_f32 v[0:1], v[0:1], v[228:229]
	v_pk_mul_f32 v[2:3], v[2:3], v[230:231]
	v_pk_mul_f32 v[4:5], v[4:5], v[244:245]
	v_pk_mul_f32 v[6:7], v[6:7], v[246:247]
	v_pk_mul_f32 v[8:9], v[8:9], v[248:249]
	v_pk_mul_f32 v[10:11], v[10:11], v[206:207]
	v_pk_mul_f32 v[12:13], v[12:13], v[252:253]
	v_pk_mul_f32 v[14:15], v[14:15], v[202:203]
	v_exp_f32_e32 v96, v96
	v_exp_f32_e32 v112, v112
	v_exp_f32_e32 v97, v97
	v_exp_f32_e32 v113, v113
	v_exp_f32_e32 v100, v100
	v_exp_f32_e32 v116, v116
	v_exp_f32_e32 v101, v101
	v_exp_f32_e32 v117, v117
	v_exp_f32_e32 v104, v104
	v_exp_f32_e32 v120, v120
	v_exp_f32_e32 v105, v105
	v_exp_f32_e32 v121, v121
	v_exp_f32_e32 v108, v108
	v_exp_f32_e32 v124, v124
	v_exp_f32_e32 v109, v109
	v_exp_f32_e32 v125, v125
	v_exp_f32_e32 v98, v98
	v_exp_f32_e32 v114, v114
	v_exp_f32_e32 v99, v99
	v_exp_f32_e32 v115, v115
	v_exp_f32_e32 v102, v102
	v_exp_f32_e32 v118, v118
	v_exp_f32_e32 v103, v103
	v_exp_f32_e32 v119, v119
	s_branch .Lfd0dB_join
.Lfd1_entry:
	v_max3_f32 v226, v96, v97, v98
	v_max3_f32 v202, v99, v100, v101
	v_max3_f32 v203, v102, v103, v104
	v_max3_f32 v211, v105, v106, v107
	v_max3_f32 v226, v226, v108, v109
	v_max3_f32 v202, v202, v110, v111
	v_max3_f32 v226, v226, v203, v211
	v_max_f32_e32 v226, v226, v202
	v_max3_f32 v227, v112, v113, v114
	v_max3_f32 v202, v115, v116, v117
	v_max3_f32 v203, v118, v119, v120
	v_max3_f32 v211, v121, v122, v123
	v_max3_f32 v227, v227, v124, v125
	v_max3_f32 v202, v202, v126, v127
	v_max3_f32 v227, v227, v203, v211
	v_max_f32_e32 v227, v227, v202
	v_max_f32_e32 v226, v226, v227
	v_cmp_lt_f32_e32 vcc, 0x41000000, v226
	s_cbranch_vccz .Lfd1_eexp
	v_mov_b32_e32 v227, v226
	s_nop 1
	v_permlane32_swap_b32_e32 v226, v227
	v_max3_f32 v226, v226, v227, v227
	s_nop 0
	v_max_f32_e32 v80, v226, v226
	v_max_f32_e32 v82, 0, v80
	s_and_saveexec_b64 s[0:1], s[6:7]
	v_exp_f32_e64 v80, -v82
	s_nop 0
	ds_write_b32 v223, v80 offset:49152
	s_or_b64 exec, exec, s[0:1]
	v_add_u32_e32 v210, s78, v224
	s_waitcnt lgkmcnt(0)
	v_add_u32_e32 v251, 0xc000, v210
	ds_read2_b32 v[228:229], v251 offset1:1
	v_add_u32_e32 v251, 0xc008, v210
	ds_read2_b32 v[230:231], v251 offset1:1
	v_add_u32_e32 v251, 0xc020, v210
	ds_read2_b32 v[244:245], v251 offset1:1
	v_add_u32_e32 v251, 0xc028, v210
	ds_read2_b32 v[246:247], v251 offset1:1
	v_add_u32_e32 v251, 0xc040, v210
	ds_read2_b32 v[248:249], v251 offset1:1
	v_add_u32_e32 v251, 0xc048, v210
	ds_read2_b32 v[206:207], v251 offset1:1
	v_add_u32_e32 v251, 0xc060, v210
	ds_read2_b32 v[252:253], v251 offset1:1
	v_add_u32_e32 v251, 0xc068, v210
	ds_read2_b32 v[202:203], v251 offset1:1
	v_add_f32_e32 v225, v225, v82
	v_xor_b32_e32 v80, 0x80000000, v225
	v_pk_add_f32 v[96:97], v[96:97], v[82:83] op_sel_hi:[1,0] neg_lo:[0,1] neg_hi:[0,1]
	v_pk_add_f32 v[112:113], v[112:113], v[82:83] op_sel_hi:[1,0] neg_lo:[0,1] neg_hi:[0,1]
	v_pk_add_f32 v[98:99], v[98:99], v[82:83] op_sel_hi:[1,0] neg_lo:[0,1] neg_hi:[0,1]
	v_pk_add_f32 v[114:115], v[114:115], v[82:83] op_sel_hi:[1,0] neg_lo:[0,1] neg_hi:[0,1]
	v_pk_add_f32 v[100:101], v[100:101], v[82:83] op_sel_hi:[1,0] neg_lo:[0,1] neg_hi:[0,1]
	v_pk_add_f32 v[116:117], v[116:117], v[82:83] op_sel_hi:[1,0] neg_lo:[0,1] neg_hi:[0,1]
	v_pk_add_f32 v[102:103], v[102:103], v[82:83] op_sel_hi:[1,0] neg_lo:[0,1] neg_hi:[0,1]
	v_pk_add_f32 v[118:119], v[118:119], v[82:83] op_sel_hi:[1,0] neg_lo:[0,1] neg_hi:[0,1]
	v_pk_add_f32 v[104:105], v[104:105], v[82:83] op_sel_hi:[1,0] neg_lo:[0,1] neg_hi:[0,1]
	v_pk_add_f32 v[120:121], v[120:121], v[82:83] op_sel_hi:[1,0] neg_lo:[0,1] neg_hi:[0,1]
	v_pk_add_f32 v[106:107], v[106:107], v[82:83] op_sel_hi:[1,0] neg_lo:[0,1] neg_hi:[0,1]
	v_pk_add_f32 v[122:123], v[122:123], v[82:83] op_sel_hi:[1,0] neg_lo:[0,1] neg_hi:[0,1]
	v_pk_add_f32 v[108:109], v[108:109], v[82:83] op_sel_hi:[1,0] neg_lo:[0,1] neg_hi:[0,1]
	v_pk_add_f32 v[124:125], v[124:125], v[82:83] op_sel_hi:[1,0] neg_lo:[0,1] neg_hi:[0,1]
	v_pk_add_f32 v[110:111], v[110:111], v[82:83] op_sel_hi:[1,0] neg_lo:[0,1] neg_hi:[0,1]
	v_pk_add_f32 v[126:127], v[126:127], v[82:83] op_sel_hi:[1,0] neg_lo:[0,1] neg_hi:[0,1]
	v_mov_b32_e32 v81, v80
	v_mov_b32_e32 v82, v80
	v_mov_b32_e32 v83, v80
	v_mov_b32_e32 v84, v80
	v_mov_b32_e32 v85, v80
	v_mov_b32_e32 v86, v80
	v_mov_b32_e32 v87, v80
	v_mov_b32_e32 v88, v80
	v_mov_b32_e32 v89, v80
	v_mov_b32_e32 v90, v80
	v_mov_b32_e32 v91, v80
	v_mov_b32_e32 v92, v80
	v_mov_b32_e32 v93, v80
	v_mov_b32_e32 v94, v80
	v_mov_b32_e32 v95, v80
	s_waitcnt lgkmcnt(0)
	v_pk_mul_f32 v[64:65], v[64:65], v[228:229]
	v_pk_mul_f32 v[66:67], v[66:67], v[230:231]
	v_pk_mul_f32 v[68:69], v[68:69], v[244:245]
	v_pk_mul_f32 v[70:71], v[70:71], v[246:247]
	v_pk_mul_f32 v[72:73], v[72:73], v[248:249]
	v_pk_mul_f32 v[74:75], v[74:75], v[206:207]
	v_pk_mul_f32 v[76:77], v[76:77], v[252:253]
	v_pk_mul_f32 v[78:79], v[78:79], v[202:203]
	v_pk_mul_f32 v[48:49], v[48:49], v[228:229]
	v_pk_mul_f32 v[50:51], v[50:51], v[230:231]
	v_pk_mul_f32 v[52:53], v[52:53], v[244:245]
	v_pk_mul_f32 v[54:55], v[54:55], v[246:247]
	v_pk_mul_f32 v[56:57], v[56:57], v[248:249]
	v_pk_mul_f32 v[58:59], v[58:59], v[206:207]
	v_pk_mul_f32 v[60:61], v[60:61], v[252:253]
	v_pk_mul_f32 v[62:63], v[62:63], v[202:203]
	v_pk_mul_f32 v[32:33], v[32:33], v[228:229]
	v_pk_mul_f32 v[34:35], v[34:35], v[230:231]
	v_pk_mul_f32 v[36:37], v[36:37], v[244:245]
	v_pk_mul_f32 v[38:39], v[38:39], v[246:247]
	v_pk_mul_f32 v[40:41], v[40:41], v[248:249]
	v_pk_mul_f32 v[42:43], v[42:43], v[206:207]
	v_pk_mul_f32 v[44:45], v[44:45], v[252:253]
	v_pk_mul_f32 v[46:47], v[46:47], v[202:203]
	v_pk_mul_f32 v[16:17], v[16:17], v[228:229]
	v_pk_mul_f32 v[18:19], v[18:19], v[230:231]
	v_pk_mul_f32 v[20:21], v[20:21], v[244:245]
	v_pk_mul_f32 v[22:23], v[22:23], v[246:247]
	v_pk_mul_f32 v[24:25], v[24:25], v[248:249]
	v_pk_mul_f32 v[26:27], v[26:27], v[206:207]
	v_pk_mul_f32 v[28:29], v[28:29], v[252:253]
	v_pk_mul_f32 v[30:31], v[30:31], v[202:203]
	v_pk_mul_f32 v[0:1], v[0:1], v[228:229]
	v_pk_mul_f32 v[2:3], v[2:3], v[230:231]
	v_pk_mul_f32 v[4:5], v[4:5], v[244:245]
	v_pk_mul_f32 v[6:7], v[6:7], v[246:247]
	v_pk_mul_f32 v[8:9], v[8:9], v[248:249]
	v_pk_mul_f32 v[10:11], v[10:11], v[206:207]
	v_pk_mul_f32 v[12:13], v[12:13], v[252:253]
	v_pk_mul_f32 v[14:15], v[14:15], v[202:203]
.Lfd1_eexp:
	v_exp_f32_e32 v96, v96
	v_exp_f32_e32 v112, v112
	v_exp_f32_e32 v97, v97
	v_exp_f32_e32 v113, v113
	v_exp_f32_e32 v100, v100
	v_exp_f32_e32 v116, v116
	v_exp_f32_e32 v101, v101
	v_exp_f32_e32 v117, v117
	v_exp_f32_e32 v104, v104
	v_exp_f32_e32 v120, v120
	v_exp_f32_e32 v105, v105
	v_exp_f32_e32 v121, v121
	v_exp_f32_e32 v108, v108
	v_exp_f32_e32 v124, v124
	v_exp_f32_e32 v109, v109
	v_exp_f32_e32 v125, v125
	v_exp_f32_e32 v98, v98
	v_exp_f32_e32 v114, v114
	v_exp_f32_e32 v99, v99
	v_exp_f32_e32 v115, v115
	v_exp_f32_e32 v102, v102
	v_exp_f32_e32 v118, v118
	v_exp_f32_e32 v103, v103
	v_exp_f32_e32 v119, v119
	v_exp_f32_e32 v106, v106
	v_exp_f32_e32 v122, v122
	v_exp_f32_e32 v107, v107
	v_exp_f32_e32 v123, v123
	v_exp_f32_e32 v110, v110
	v_exp_f32_e32 v126, v126
	v_exp_f32_e32 v111, v111
	v_exp_f32_e32 v127, v127
	v_cvt_pk_fp8_f32 v160, v96, v97
	v_cvt_pk_fp8_f32 v164, v112, v113
	v_cvt_pk_fp8_f32 v161, v100, v101
	v_cvt_pk_fp8_f32 v165, v116, v117
	v_cvt_pk_fp8_f32 v162, v104, v105
	v_cvt_pk_fp8_f32 v166, v120, v121
	v_cvt_pk_fp8_f32 v163, v108, v109
	v_cvt_pk_fp8_f32 v167, v124, v125
	v_cvt_pk_fp8_f32 v160, v98, v99 op_sel:[0,0,1]
	v_cvt_pk_fp8_f32 v164, v114, v115 op_sel:[0,0,1]
	v_cvt_pk_fp8_f32 v161, v102, v103 op_sel:[0,0,1]
	v_cvt_pk_fp8_f32 v165, v118, v119 op_sel:[0,0,1]
	v_cvt_pk_fp8_f32 v162, v106, v107 op_sel:[0,0,1]
	v_cvt_pk_fp8_f32 v166, v122, v123 op_sel:[0,0,1]
	v_cvt_pk_fp8_f32 v163, v110, v111 op_sel:[0,0,1]
	v_cvt_pk_fp8_f32 v167, v126, v127 op_sel:[0,0,1]
	v_add_u32_e32 v232, s91, v222
	v_add_u32_e32 v233, s91, v221
	s_add_i32 s32, s86, s2
	s_add_i32 s50, s32, -1
	s_mov_b32 s51, 0
	s_lshl_b64 s[50:51], s[50:51], 6
	s_add_u32 s50, s97, s50
	s_addc_u32 s51, s87, s51
	s_add_i32 m0, s79, 0x4000
	s_nop 0
	global_load_lds_dwordx4 v218, s[50:51]
	ds_read_b128 v[144:147], v232 offset:8192
	ds_read_b128 v[148:151], v233 offset:8192
	ds_read_b128 v[152:155], v232 offset:10240
	ds_read_b128 v[156:159], v233 offset:10240
	ds_read_b128 v[176:179], v232 offset:24576
	ds_read_b128 v[180:183], v233 offset:24576
	ds_read_b128 v[168:171], v232 offset:26624
	ds_read_b128 v[172:175], v233 offset:26624
	ds_read_b128 v[192:195], v232 offset:28672
	ds_read_b128 v[196:199], v233 offset:28672
	ds_read_b128 v[184:187], v232 offset:30720
	ds_read_b128 v[188:191], v233 offset:30720
	s_add_i32 s32, s86, s2
	s_add_i32 s32, s32, 1
	s_add_i32 s50, s32, -1
	s_mov_b32 s51, 0
	s_lshl_b64 s[50:51], s[50:51], 6
	s_add_u32 s50, s97, s50
	s_addc_u32 s51, s87, s51
	s_waitcnt vmcnt(2)
	s_waitcnt lgkmcnt(0)
	s_barrier
	s_mov_b32 s13, s12
	s_add_i32 s12, s12, 1
	s_and_b32 s12, s12, 3
	s_add_i32 s2, s2, 1
	s_add_i32 s3, s3, 64
	s_cmp_lt_u32 s2, s16
	s_cbranch_scc0 .Lfd1_drainA
.Lfd1_it3:
	v_mfma_scale_f32_32x32x64_f8f6f4 v[96:111], v[144:151], v[128:135], v[80:95], v220, v220 op_sel_hi:[0,0,0]
	s_add_i32 m0, s79, 0x6000
	s_nop 0
	global_load_lds_dwordx4 v218, s[50:51]
	s_add_i32 s32, s86, s2
	s_add_i32 s32, s32, 1
	s_add_i32 s50, s32, -1
	v_mfma_scale_f32_32x32x64_f8f6f4 v[112:127], v[152:159], v[128:135], v[80:95], v220, v220 op_sel_hi:[0,0,0]
	s_mov_b32 s51, 0
	s_lshl_b64 s[50:51], s[50:51], 6
	s_add_u32 s50, s97, s50
	s_addc_u32 s51, s87, s51
	v_mfma_scale_f32_32x32x64_f8f6f4 v[0:15], v[160:167], v[136:143], v[0:15], v219, v219 op_sel_hi:[0,0,0]
	ds_read_b128 v[144:147], v232 offset:12288
	ds_read_b128 v[148:151], v233 offset:12288
	ds_read_b128 v[152:155], v232 offset:14336
	ds_read_b128 v[156:159], v233 offset:14336
	v_max3_f32 v226, v96, v97, v98
	v_max3_f32 v202, v99, v100, v101
	v_max3_f32 v203, v102, v103, v104
	v_max3_f32 v211, v105, v106, v107
	v_max3_f32 v226, v226, v108, v109
	v_max3_f32 v202, v202, v110, v111
	v_max3_f32 v226, v226, v203, v211
	v_max_f32_e32 v226, v226, v202
	v_mfma_scale_f32_32x32x64_f8f6f4 v[64:79], v[160:167], v[176:183], v[64:79], v219, v219 op_sel_hi:[0,0,0]
	v_max3_f32 v227, v112, v113, v114
	v_max3_f32 v202, v115, v116, v117
	v_max3_f32 v203, v118, v119, v120
	v_max3_f32 v211, v121, v122, v123
	v_max3_f32 v227, v227, v124, v125
	v_max3_f32 v202, v202, v126, v127
	v_max3_f32 v227, v227, v203, v211
	v_max_f32_e32 v227, v227, v202
	v_max_f32_e32 v226, v226, v227
	v_cmp_lt_f32_e32 vcc, 0x41000000, v226
	s_cbranch_vccnz .Lfd1_3_rare
	v_mfma_scale_f32_32x32x64_f8f6f4 v[48:63], v[160:167], v[168:175], v[48:63], v219, v219 op_sel_hi:[0,0,0]
	ds_read_b128 v[176:179], v232 offset:32768
	ds_read_b128 v[180:183], v233 offset:32768
	v_exp_f32_e32 v96, v96
	v_exp_f32_e32 v112, v112
	v_exp_f32_e32 v97, v97
	v_exp_f32_e32 v113, v113
	v_exp_f32_e32 v100, v100
	v_exp_f32_e32 v116, v116
	v_exp_f32_e32 v101, v101
	v_exp_f32_e32 v117, v117
	v_mfma_scale_f32_32x32x64_f8f6f4 v[32:47], v[160:167], v[192:199], v[32:47], v219, v219 op_sel_hi:[0,0,0]
	ds_read_b128 v[168:171], v232 offset:34816
	ds_read_b128 v[172:175], v233 offset:34816
	v_exp_f32_e32 v104, v104
	v_exp_f32_e32 v120, v120
	v_exp_f32_e32 v105, v105
	v_exp_f32_e32 v121, v121
	v_exp_f32_e32 v108, v108
	v_exp_f32_e32 v124, v124
	v_exp_f32_e32 v109, v109
	v_exp_f32_e32 v125, v125
	v_mfma_scale_f32_32x32x64_f8f6f4 v[16:31], v[160:167], v[184:191], v[16:31], v219, v219 op_sel_hi:[0,0,0]
	ds_read_b128 v[192:195], v232 offset:36864
	ds_read_b128 v[196:199], v233 offset:36864
	v_exp_f32_e32 v98, v98
	v_exp_f32_e32 v114, v114
	v_exp_f32_e32 v99, v99
	v_exp_f32_e32 v115, v115
	v_exp_f32_e32 v102, v102
	v_exp_f32_e32 v118, v118
	v_exp_f32_e32 v103, v103
	v_exp_f32_e32 v119, v119
	ds_read_b128 v[184:187], v232 offset:38912
	ds_read_b128 v[188:191], v233 offset:38912
.Lfd1_3_join:
	v_exp_f32_e32 v106, v106
	v_exp_f32_e32 v122, v122
	v_exp_f32_e32 v107, v107
	v_exp_f32_e32 v123, v123
	v_exp_f32_e32 v110, v110
	v_exp_f32_e32 v126, v126
	v_exp_f32_e32 v111, v111
	v_exp_f32_e32 v127, v127
	v_cvt_pk_fp8_f32 v236, v96, v97
	v_cvt_pk_fp8_f32 v240, v112, v113
	v_cvt_pk_fp8_f32 v237, v100, v101
	v_cvt_pk_fp8_f32 v241, v116, v117
	v_cvt_pk_fp8_f32 v238, v104, v105
	v_cvt_pk_fp8_f32 v242, v120, v121
	v_cvt_pk_fp8_f32 v239, v108, v109
	v_cvt_pk_fp8_f32 v243, v124, v125
	v_cvt_pk_fp8_f32 v236, v98, v99 op_sel:[0,0,1]
	v_cvt_pk_fp8_f32 v240, v114, v115 op_sel:[0,0,1]
	v_cvt_pk_fp8_f32 v237, v102, v103 op_sel:[0,0,1]
	v_cvt_pk_fp8_f32 v241, v118, v119 op_sel:[0,0,1]
	v_cvt_pk_fp8_f32 v238, v106, v107 op_sel:[0,0,1]
	v_cvt_pk_fp8_f32 v242, v122, v123 op_sel:[0,0,1]
	v_cvt_pk_fp8_f32 v239, v110, v111 op_sel:[0,0,1]
	v_cvt_pk_fp8_f32 v243, v126, v127 op_sel:[0,0,1]
	s_waitcnt vmcnt(2)
	s_waitcnt lgkmcnt(0)
	s_barrier
	s_mov_b32 s13, s12
	s_add_i32 s12, s12, 1
	s_and_b32 s12, s12, 3
	s_add_i32 s2, s2, 1
	s_add_i32 s3, s3, 64
	s_cmp_lt_u32 s2, s16
	s_cbranch_scc1 .Lfd1_it0
	s_branch .Lfd1_drainB
.Lfd1_it0:
	v_mfma_scale_f32_32x32x64_f8f6f4 v[96:111], v[144:151], v[128:135], v[80:95], v220, v220 op_sel_hi:[0,0,0]
	s_add_i32 m0, s79, 0x8000
	s_nop 0
	global_load_lds_dwordx4 v218, s[50:51]
	s_add_i32 s32, s86, s2
	s_add_i32 s32, s32, 1
	s_add_i32 s50, s32, -1
	v_mfma_scale_f32_32x32x64_f8f6f4 v[112:127], v[152:159], v[128:135], v[80:95], v220, v220 op_sel_hi:[0,0,0]
	s_mov_b32 s51, 0
	s_lshl_b64 s[50:51], s[50:51], 6
	s_add_u32 s50, s97, s50
	s_addc_u32 s51, s87, s51
	v_mfma_scale_f32_32x32x64_f8f6f4 v[0:15], v[236:243], v[136:143], v[0:15], v219, v219 op_sel_hi:[0,0,0]
	ds_read_b128 v[144:147], v232
	ds_read_b128 v[148:151], v233
	ds_read_b128 v[152:155], v232 offset:2048
	ds_read_b128 v[156:159], v233 offset:2048
	v_max3_f32 v226, v96, v97, v98
	v_max3_f32 v202, v99, v100, v101
	v_max3_f32 v203, v102, v103, v104
	v_max3_f32 v211, v105, v106, v107
	v_max3_f32 v226, v226, v108, v109
	v_max3_f32 v202, v202, v110, v111
	v_max3_f32 v226, v226, v203, v211
	v_max_f32_e32 v226, v226, v202
	v_mfma_scale_f32_32x32x64_f8f6f4 v[64:79], v[236:243], v[176:183], v[64:79], v219, v219 op_sel_hi:[0,0,0]
	v_max3_f32 v227, v112, v113, v114
	v_max3_f32 v202, v115, v116, v117
	v_max3_f32 v203, v118, v119, v120
	v_max3_f32 v211, v121, v122, v123
	v_max3_f32 v227, v227, v124, v125
	v_max3_f32 v202, v202, v126, v127
	v_max3_f32 v227, v227, v203, v211
	v_max_f32_e32 v227, v227, v202
	v_max_f32_e32 v226, v226, v227
	v_cmp_lt_f32_e32 vcc, 0x41000000, v226
	s_cbranch_vccnz .Lfd1_0_rare
	v_mfma_scale_f32_32x32x64_f8f6f4 v[48:63], v[236:243], v[168:175], v[48:63], v219, v219 op_sel_hi:[0,0,0]
	ds_read_b128 v[176:179], v232 offset:40960
	ds_read_b128 v[180:183], v233 offset:40960
	v_exp_f32_e32 v96, v96
	v_exp_f32_e32 v112, v112
	v_exp_f32_e32 v97, v97
	v_exp_f32_e32 v113, v113
	v_exp_f32_e32 v100, v100
	v_exp_f32_e32 v116, v116
	v_exp_f32_e32 v101, v101
	v_exp_f32_e32 v117, v117
	v_mfma_scale_f32_32x32x64_f8f6f4 v[32:47], v[236:243], v[192:199], v[32:47], v219, v219 op_sel_hi:[0,0,0]
	ds_read_b128 v[168:171], v232 offset:43008
	ds_read_b128 v[172:175], v233 offset:43008
	v_exp_f32_e32 v104, v104
	v_exp_f32_e32 v120, v120
	v_exp_f32_e32 v105, v105
	v_exp_f32_e32 v121, v121
	v_exp_f32_e32 v108, v108
	v_exp_f32_e32 v124, v124
	v_exp_f32_e32 v109, v109
	v_exp_f32_e32 v125, v125
	v_mfma_scale_f32_32x32x64_f8f6f4 v[16:31], v[236:243], v[184:191], v[16:31], v219, v219 op_sel_hi:[0,0,0]
	ds_read_b128 v[192:195], v232 offset:45056
	ds_read_b128 v[196:199], v233 offset:45056
	v_exp_f32_e32 v98, v98
	v_exp_f32_e32 v114, v114
	v_exp_f32_e32 v99, v99
	v_exp_f32_e32 v115, v115
	v_exp_f32_e32 v102, v102
	v_exp_f32_e32 v118, v118
	v_exp_f32_e32 v103, v103
	v_exp_f32_e32 v119, v119
	ds_read_b128 v[184:187], v232 offset:47104
	ds_read_b128 v[188:191], v233 offset:47104
.Lfd1_0_join:
	v_exp_f32_e32 v106, v106
	v_exp_f32_e32 v122, v122
	v_exp_f32_e32 v107, v107
	v_exp_f32_e32 v123, v123
	v_exp_f32_e32 v110, v110
	v_exp_f32_e32 v126, v126
	v_exp_f32_e32 v111, v111
	v_exp_f32_e32 v127, v127
	v_cvt_pk_fp8_f32 v160, v96, v97
	v_cvt_pk_fp8_f32 v164, v112, v113
	v_cvt_pk_fp8_f32 v161, v100, v101
	v_cvt_pk_fp8_f32 v165, v116, v117
	v_cvt_pk_fp8_f32 v162, v104, v105
	v_cvt_pk_fp8_f32 v166, v120, v121
	v_cvt_pk_fp8_f32 v163, v108, v109
	v_cvt_pk_fp8_f32 v167, v124, v125
	v_cvt_pk_fp8_f32 v160, v98, v99 op_sel:[0,0,1]
	v_cvt_pk_fp8_f32 v164, v114, v115 op_sel:[0,0,1]
	v_cvt_pk_fp8_f32 v161, v102, v103 op_sel:[0,0,1]
	v_cvt_pk_fp8_f32 v165, v118, v119 op_sel:[0,0,1]
	v_cvt_pk_fp8_f32 v162, v106, v107 op_sel:[0,0,1]
	v_cvt_pk_fp8_f32 v166, v122, v123 op_sel:[0,0,1]
	v_cvt_pk_fp8_f32 v163, v110, v111 op_sel:[0,0,1]
	v_cvt_pk_fp8_f32 v167, v126, v127 op_sel:[0,0,1]
	s_waitcnt vmcnt(2)
	s_waitcnt lgkmcnt(0)
	s_barrier
	s_mov_b32 s13, s12
	s_add_i32 s12, s12, 1
	s_and_b32 s12, s12, 3
	s_add_i32 s2, s2, 1
	s_add_i32 s3, s3, 64
	s_cmp_lt_u32 s2, s16
	s_cbranch_scc1 .Lfd1_it1
	s_branch .Lfd1_drainA
.Lfd1_it1:
	v_mfma_scale_f32_32x32x64_f8f6f4 v[96:111], v[144:151], v[128:135], v[80:95], v220, v220 op_sel_hi:[0,0,0]
	s_add_i32 m0, s79, 0xa000
	s_nop 0
	global_load_lds_dwordx4 v218, s[50:51]
	s_add_i32 s32, s86, s2
	s_add_i32 s32, s32, 1
	s_add_i32 s50, s32, -1
	v_mfma_scale_f32_32x32x64_f8f6f4 v[112:127], v[152:159], v[128:135], v[80:95], v220, v220 op_sel_hi:[0,0,0]
	s_mov_b32 s51, 0
	s_lshl_b64 s[50:51], s[50:51], 6
	s_add_u32 s50, s97, s50
	s_addc_u32 s51, s87, s51
	v_mfma_scale_f32_32x32x64_f8f6f4 v[0:15], v[160:167], v[136:143], v[0:15], v219, v219 op_sel_hi:[0,0,0]
	ds_read_b128 v[144:147], v232 offset:4096
	ds_read_b128 v[148:151], v233 offset:4096
	ds_read_b128 v[152:155], v232 offset:6144
	ds_read_b128 v[156:159], v233 offset:6144
	v_max3_f32 v226, v96, v97, v98
	v_max3_f32 v202, v99, v100, v101
	v_max3_f32 v203, v102, v103, v104
	v_max3_f32 v211, v105, v106, v107
	v_max3_f32 v226, v226, v108, v109
	v_max3_f32 v202, v202, v110, v111
	v_max3_f32 v226, v226, v203, v211
	v_max_f32_e32 v226, v226, v202
	v_mfma_scale_f32_32x32x64_f8f6f4 v[64:79], v[160:167], v[176:183], v[64:79], v219, v219 op_sel_hi:[0,0,0]
	v_max3_f32 v227, v112, v113, v114
	v_max3_f32 v202, v115, v116, v117
	v_max3_f32 v203, v118, v119, v120
	v_max3_f32 v211, v121, v122, v123
	v_max3_f32 v227, v227, v124, v125
	v_max3_f32 v202, v202, v126, v127
	v_max3_f32 v227, v227, v203, v211
	v_max_f32_e32 v227, v227, v202
	v_max_f32_e32 v226, v226, v227
	v_cmp_lt_f32_e32 vcc, 0x41000000, v226
	s_cbranch_vccnz .Lfd1_1_rare
	v_mfma_scale_f32_32x32x64_f8f6f4 v[48:63], v[160:167], v[168:175], v[48:63], v219, v219 op_sel_hi:[0,0,0]
	ds_read_b128 v[176:179], v232 offset:16384
	ds_read_b128 v[180:183], v233 offset:16384
	v_exp_f32_e32 v96, v96
	v_exp_f32_e32 v112, v112
	v_exp_f32_e32 v97, v97
	v_exp_f32_e32 v113, v113
	v_exp_f32_e32 v100, v100
	v_exp_f32_e32 v116, v116
	v_exp_f32_e32 v101, v101
	v_exp_f32_e32 v117, v117
	v_mfma_scale_f32_32x32x64_f8f6f4 v[32:47], v[160:167], v[192:199], v[32:47], v219, v219 op_sel_hi:[0,0,0]
	ds_read_b128 v[168:171], v232 offset:18432
	ds_read_b128 v[172:175], v233 offset:18432
	v_exp_f32_e32 v104, v104
	v_exp_f32_e32 v120, v120
	v_exp_f32_e32 v105, v105
	v_exp_f32_e32 v121, v121
	v_exp_f32_e32 v108, v108
	v_exp_f32_e32 v124, v124
	v_exp_f32_e32 v109, v109
	v_exp_f32_e32 v125, v125
	v_mfma_scale_f32_32x32x64_f8f6f4 v[16:31], v[160:167], v[184:191], v[16:31], v219, v219 op_sel_hi:[0,0,0]
	ds_read_b128 v[192:195], v232 offset:20480
	ds_read_b128 v[196:199], v233 offset:20480
	v_exp_f32_e32 v98, v98
	v_exp_f32_e32 v114, v114
	v_exp_f32_e32 v99, v99
	v_exp_f32_e32 v115, v115
	v_exp_f32_e32 v102, v102
	v_exp_f32_e32 v118, v118
	v_exp_f32_e32 v103, v103
	v_exp_f32_e32 v119, v119
	ds_read_b128 v[184:187], v232 offset:22528
	ds_read_b128 v[188:191], v233 offset:22528

.Lfd1_it2:
	v_mfma_scale_f32_32x32x64_f8f6f4 v[96:111], v[144:151], v[128:135], v[80:95], v220, v220 op_sel_hi:[0,0,0]
	s_add_i32 m0, s79, 0x4000
	s_nop 0
	global_load_lds_dwordx4 v218, s[50:51]
	s_add_i32 s32, s86, s2
	s_add_i32 s32, s32, 1
	s_add_i32 s50, s32, -1
	v_mfma_scale_f32_32x32x64_f8f6f4 v[112:127], v[152:159], v[128:135], v[80:95], v220, v220 op_sel_hi:[0,0,0]
	s_mov_b32 s51, 0
	s_lshl_b64 s[50:51], s[50:51], 6
	s_add_u32 s50, s97, s50
	s_addc_u32 s51, s87, s51
	v_mfma_scale_f32_32x32x64_f8f6f4 v[0:15], v[236:243], v[136:143], v[0:15], v219, v219 op_sel_hi:[0,0,0]
	ds_read_b128 v[144:147], v232 offset:8192
	ds_read_b128 v[148:151], v233 offset:8192
	ds_read_b128 v[152:155], v232 offset:10240
	ds_read_b128 v[156:159], v233 offset:10240
	v_max3_f32 v226, v96, v97, v98
	v_max3_f32 v202, v99, v100, v101
	v_max3_f32 v203, v102, v103, v104
	v_max3_f32 v211, v105, v106, v107
	v_max3_f32 v226, v226, v108, v109
	v_max3_f32 v202, v202, v110, v111
	v_max3_f32 v226, v226, v203, v211
	v_max_f32_e32 v226, v226, v202
	v_mfma_scale_f32_32x32x64_f8f6f4 v[64:79], v[236:243], v[176:183], v[64:79], v219, v219 op_sel_hi:[0,0,0]
	v_max3_f32 v227, v112, v113, v114
	v_max3_f32 v202, v115, v116, v117
	v_max3_f32 v203, v118, v119, v120
	v_max3_f32 v211, v121, v122, v123
	v_max3_f32 v227, v227, v124, v125
	v_max3_f32 v202, v202, v126, v127
	v_max3_f32 v227, v227, v203, v211
	v_max_f32_e32 v227, v227, v202
	v_max_f32_e32 v226, v226, v227
	v_cmp_lt_f32_e32 vcc, 0x41000000, v226
	s_cbranch_vccnz .Lfd1_2_rare
	v_mfma_scale_f32_32x32x64_f8f6f4 v[48:63], v[236:243], v[168:175], v[48:63], v219, v219 op_sel_hi:[0,0,0]
	ds_read_b128 v[176:179], v232 offset:24576
	ds_read_b128 v[180:183], v233 offset:24576
	v_exp_f32_e32 v96, v96
	v_exp_f32_e32 v112, v112
	v_exp_f32_e32 v97, v97
	v_exp_f32_e32 v113, v113
	v_exp_f32_e32 v100, v100
	v_exp_f32_e32 v116, v116
	v_exp_f32_e32 v101, v101
	v_exp_f32_e32 v117, v117
	v_mfma_scale_f32_32x32x64_f8f6f4 v[32:47], v[236:243], v[192:199], v[32:47], v219, v219 op_sel_hi:[0,0,0]
	ds_read_b128 v[168:171], v232 offset:26624
	ds_read_b128 v[172:175], v233 offset:26624
	v_exp_f32_e32 v104, v104
	v_exp_f32_e32 v120, v120
	v_exp_f32_e32 v105, v105
	v_exp_f32_e32 v121, v121
	v_exp_f32_e32 v108, v108
	v_exp_f32_e32 v124, v124
	v_exp_f32_e32 v109, v109
	v_exp_f32_e32 v125, v125
	v_mfma_scale_f32_32x32x64_f8f6f4 v[16:31], v[236:243], v[184:191], v[16:31], v219, v219 op_sel_hi:[0,0,0]
	ds_read_b128 v[192:195], v232 offset:28672
	ds_read_b128 v[196:199], v233 offset:28672
	v_exp_f32_e32 v98, v98
	v_exp_f32_e32 v114, v114
	v_exp_f32_e32 v99, v99
	v_exp_f32_e32 v115, v115
	v_exp_f32_e32 v102, v102
	v_exp_f32_e32 v118, v118
	v_exp_f32_e32 v103, v103
	v_exp_f32_e32 v119, v119
	ds_read_b128 v[184:187], v232 offset:30720
	ds_read_b128 v[188:191], v233 offset:30720

.LBB0_912:
	s_lshl_b32 s18, s15, 7
	s_lshl_b32 s13, s13, 18
	s_add_i32 s33, s18, s13
	s_add_u32 s39, s76, 0x79000000
	s_addc_u32 s40, s77, 0
	s_lshl_b64 s[20:21], s[36:37], 2
	s_add_u32 s36, s10, s20
	s_addc_u32 s41, s11, s21
	s_add_u32 s10, s76, s20
	s_addc_u32 s11, s77, s21
	s_add_u32 s42, s10, 0x9f400000
	s_addc_u32 s43, s11, 0
	s_add_u32 s44, s76, 0x9f800000
	s_addc_u32 s45, s77, 0
	s_lshl_b32 s10, s75, 5
	s_and_b32 s46, s10, 0x60
	s_lshl_b32 s13, s12, 13
	s_lshl_b32 s15, s46, 7
	s_add_i32 s47, s27, 0x18000
	s_add_i32 s48, s27, 0x1a000
	s_add_u32 s20, s76, 0x60800080
	s_addc_u32 s21, s77, 0
	s_add_i32 s49, s27, 0x8000
	s_add_i32 s50, s27, 0xa000
	s_add_i32 s51, s27, 0x1c000
	s_add_i32 s52, s27, 0x1e000
	s_add_i32 s53, s91, 0x10000
	s_add_i32 s54, s91, 0x14000
	s_add_i32 s55, s27, 0xc000
	s_add_i32 s56, s91, 0x18000
	s_add_i32 s57, s91, 0x1c000
	s_cmp_lt_u32 s75, 4
	s_cselect_b64 s[10:11], -1, 0
	s_lshl_b32 s58, s12, 8
	s_lshl_b32 s59, s12, 16
	v_readlane_b32 s12, v254, 34
	v_readlane_b32 s17, v254, 35
	s_add_i32 s60, s27, 0xe000
	s_ashr_i32 s61, s12, 31
	s_ashr_i32 s62, s17, 31
	s_ashr_i32 s63, s12, 3
	s_add_u32 s4, s4, 0x80
	s_waitcnt vmcnt(2)
	s_barrier
	s_addc_u32 s5, s5, 0
	s_mov_b32 m0, s47
	s_nop 4
	global_load_lds_dwordx4 v171, s[4:5]
	s_mov_b32 m0, s48
	s_nop 4
	global_load_lds_dwordx4 v173, s[4:5]
	s_mov_b32 m0, s49
	s_nop 4
	global_load_lds_dwordx4 v136, s[20:21]
	s_add_i32 s4, s70, 0x100080
	s_mov_b32 m0, s50
	s_nop 4
	global_load_lds_dwordx4 v137, s[20:21]
	s_add_u32 s4, s25, s4
	s_addc_u32 s5, s26, 0
	s_mov_b32 m0, s51
	s_nop 4
	global_load_lds_dwordx4 v171, s[4:5]
	v_and_b32_e32 v1, 15, v0
	v_and_b32_e32 v2, 48, v0
	v_lshlrev_b32_e32 v0, 2, v0
	s_mov_b32 m0, s52
	s_nop 4
	global_load_lds_dwordx4 v173, s[4:5]
	v_lshl_or_b32 v1, v1, 6, v2
	v_and_b32_e32 v0, 32, v0
	s_waitcnt vmcnt(6)
	v_bitop3_b32 v128, v1, s13, v0 bitop3:0xde
	v_bitop3_b32 v174, v1, s15, v0 bitop3:0xde
	s_mov_b32 s15, 0
	v_add_u32_e32 v175, s91, v128
	s_barrier
	s_branch .LBB0_915

.LBB0_935:
	s_and_b64 s[4:5], s[12:13], exec
	s_cselect_b32 s18, s67, s70
	s_add_i32 s4, s66, 0x80
	v_add_u32_e32 v128, s66, v168
	v_add_u32_e32 v130, s4, v168
	v_add_u32_e32 v132, s66, v169
	v_add_u32_e32 v134, s4, v169
	v_ashrrev_i32_e32 v129, 31, v128
	v_ashrrev_i32_e32 v131, 31, v130
	v_ashrrev_i32_e32 v133, 31, v132
	v_ashrrev_i32_e32 v135, 31, v134
	v_lshl_add_u64 v[128:129], v[128:129], 2, s[6:7]
	v_lshl_add_u64 v[130:131], v[130:131], 2, s[6:7]
	v_lshl_add_u64 v[132:133], v[132:133], 2, s[6:7]
	v_lshl_add_u64 v[134:135], v[134:135], 2, s[6:7]
	s_add_i32 s19, s70, 0x100
	s_mov_b32 s21, -2
	s_mov_b64 s[16:17], 0
	v_mov_b32_e32 v176, v136
	v_mov_b32_e32 v178, v137
	v_mov_b32_e32 v177, v138
	v_mov_b32_e32 v179, v139
	s_cmp_eq_u32 s21, 4
	s_cselect_b64 s[4:5], -1, 0
	s_and_b64 s[14:15], s[12:13], s[4:5]
	s_andn2_b64 vcc, exec, s[14:15]
	s_cbranch_vccnz .Lpeel_g1_938
	global_load_dword v140, v[128:129], off
	global_load_dword v141, v[130:131], off
	global_load_dword v142, v[132:133], off
	global_load_dword v143, v[134:135], off
	s_waitcnt vmcnt(3)
	v_lshl_add_u32 v176, v140, 10, v170
	s_waitcnt vmcnt(2)
	v_lshl_add_u32 v177, v141, 10, v170
	s_waitcnt vmcnt(1)
	v_lshl_add_u32 v178, v142, 10, v172
	s_waitcnt vmcnt(0)
	v_lshl_add_u32 v179, v143, 10, v172
.Lpeel_g1_938:
	v_add_u32_e32 v152, s53, v174
	v_add_u32_e32 v180, s54, v174
	ds_read_b128 v[140:143], v152
	ds_read_b128 v[144:147], v152 offset:1024
	ds_read_b128 v[148:151], v152 offset:2048
	ds_read_b128 v[152:155], v152 offset:3072
	ds_read_b128 v[156:159], v180
	ds_read_b128 v[160:163], v180 offset:1024
	ds_read_b128 v[164:167], v180 offset:2048
	ds_read_b128 v[180:183], v180 offset:3072
	s_add_u32 s14, s16, 0x100
	s_addc_u32 s15, s17, 0
	s_and_b64 s[70:71], s[4:5], exec
	s_cselect_b32 s72, 0, s14
	s_add_i32 s73, s19, s16
	s_and_b64 s[70:71], s[4:5], exec
	s_cselect_b32 s70, s18, s73
	s_add_i32 s71, s70, 0x80
	v_cndmask_b32_e64 v200, v136, v176, s[4:5]
	v_cndmask_b32_e64 v218, v138, v177, s[4:5]
	v_cndmask_b32_e64 v219, v137, v178, s[4:5]
	v_cndmask_b32_e64 v220, v139, v179, s[4:5]
	ds_read_b128 v[184:187], v175
	ds_read_b128 v[188:191], v175 offset:1024
	ds_read_b128 v[192:195], v175 offset:2048
	ds_read_b128 v[196:199], v175 offset:3072
	ds_read_b128 v[202:205], v175 offset:4096
	ds_read_b128 v[206:209], v175 offset:5120
	ds_read_b128 v[210:213], v175 offset:6144
	ds_read_b128 v[214:217], v175 offset:7168
	s_add_u32 s4, s2, s16
	s_addc_u32 s5, s3, s17
	s_add_u32 s4, s4, 0x80
	s_addc_u32 s5, s5, 0
	s_mov_b32 m0, s55
	s_nop 4
	global_load_lds_dwordx4 v138, s[4:5]
	s_mov_b32 m0, s60
	s_nop 4
	global_load_lds_dwordx4 v139, s[4:5]
	s_waitcnt vmcnt(8)
	s_waitcnt lgkmcnt(0)
	s_barrier
	s_setprio 1
	s_waitcnt lgkmcnt(7)
	v_mfma_i32_16x16x64_i8 v[120:123], v[140:143], v[184:187], 0
	v_mfma_i32_16x16x64_i8 v[112:115], v[148:151], v[184:187], 0
	s_waitcnt lgkmcnt(5)
	v_mfma_i32_16x16x64_i8 v[104:107], v[140:143], v[192:195], 0
	v_mfma_i32_16x16x64_i8 v[96:99], v[148:151], v[192:195], 0
	s_waitcnt lgkmcnt(3)
	v_mfma_i32_16x16x64_i8 v[88:91], v[140:143], v[202:205], 0
	v_mfma_i32_16x16x64_i8 v[80:83], v[148:151], v[202:205], 0
	s_waitcnt lgkmcnt(1)
	v_mfma_i32_16x16x64_i8 v[72:75], v[140:143], v[210:213], 0
	v_mfma_i32_16x16x64_i8 v[64:67], v[148:151], v[210:213], 0
	v_mfma_i32_16x16x64_i8 v[120:123], v[144:147], v[188:191], v[120:123]
	v_mfma_i32_16x16x64_i8 v[112:115], v[152:155], v[188:191], v[112:115]
	v_mfma_i32_16x16x64_i8 v[104:107], v[144:147], v[196:199], v[104:107]
	v_mfma_i32_16x16x64_i8 v[96:99], v[152:155], v[196:199], v[96:99]
	v_mfma_i32_16x16x64_i8 v[88:91], v[144:147], v[206:209], v[88:91]
	v_mfma_i32_16x16x64_i8 v[80:83], v[152:155], v[206:209], v[80:83]
	s_waitcnt lgkmcnt(0)
	v_mfma_i32_16x16x64_i8 v[72:75], v[144:147], v[214:217], v[72:75]
	v_mfma_i32_16x16x64_i8 v[64:67], v[152:155], v[214:217], v[64:67]
	s_setprio 0
	s_setprio 1
	v_mfma_i32_16x16x64_i8 v[124:127], v[156:159], v[184:187], 0
	v_mfma_i32_16x16x64_i8 v[116:119], v[164:167], v[184:187], 0
	v_mfma_i32_16x16x64_i8 v[108:111], v[156:159], v[192:195], 0
	v_mfma_i32_16x16x64_i8 v[100:103], v[164:167], v[192:195], 0
	v_mfma_i32_16x16x64_i8 v[92:95], v[156:159], v[202:205], 0
	v_mfma_i32_16x16x64_i8 v[84:87], v[164:167], v[202:205], 0
	v_mfma_i32_16x16x64_i8 v[76:79], v[156:159], v[210:213], 0
	v_mfma_i32_16x16x64_i8 v[68:71], v[164:167], v[210:213], 0
	v_mfma_i32_16x16x64_i8 v[124:127], v[160:163], v[188:191], v[124:127]
	v_mfma_i32_16x16x64_i8 v[116:119], v[180:183], v[188:191], v[116:119]
	v_mfma_i32_16x16x64_i8 v[108:111], v[160:163], v[196:199], v[108:111]
	v_mfma_i32_16x16x64_i8 v[100:103], v[180:183], v[196:199], v[100:103]
	v_mfma_i32_16x16x64_i8 v[92:95], v[160:163], v[206:209], v[92:95]
	v_mfma_i32_16x16x64_i8 v[84:87], v[180:183], v[206:209], v[84:87]
	v_mfma_i32_16x16x64_i8 v[76:79], v[160:163], v[214:217], v[76:79]
	v_mfma_i32_16x16x64_i8 v[68:71], v[180:183], v[214:217], v[68:71]
	s_setprio 0
	s_barrier
	s_add_u32 s4, s25, s70
	ds_read_b128 v[184:187], v175 offset:16384
	ds_read_b128 v[188:191], v175 offset:17408
	ds_read_b128 v[192:195], v175 offset:18432
	ds_read_b128 v[196:199], v175 offset:19456
	ds_read_b128 v[202:205], v175 offset:20480
	ds_read_b128 v[206:209], v175 offset:21504
	ds_read_b128 v[210:213], v175 offset:22528
	ds_read_b128 v[214:217], v175 offset:23552
	s_addc_u32 s5, s26, 0
	s_mov_b32 m0, s28
	s_nop 4
	global_load_lds_dwordx4 v171, s[4:5]
	s_mov_b32 m0, s29
	s_nop 4
	global_load_lds_dwordx4 v173, s[4:5]
	s_add_i32 s4, s70, 0x100000
	s_add_u32 s4, s25, s4
	s_addc_u32 s5, s26, 0
	s_mov_b32 m0, s30
	s_nop 4
	global_load_lds_dwordx4 v171, s[4:5]
	s_mov_b32 m0, s31
	s_nop 4
	global_load_lds_dwordx4 v173, s[4:5]
	s_add_u32 s4, s2, s72
	s_addc_u32 s5, s3, 0
	s_mov_b32 m0, s27
	s_nop 4
	global_load_lds_dwordx4 v200, s[4:5]
	s_mov_b32 m0, s34
	s_nop 4
	global_load_lds_dwordx4 v219, s[4:5]
	s_waitcnt vmcnt(8)
	s_waitcnt lgkmcnt(0)
	s_barrier
	s_setprio 1
	s_waitcnt lgkmcnt(7)
	v_mfma_i32_16x16x64_i8 v[56:59], v[140:143], v[184:187], 0
	v_mfma_i32_16x16x64_i8 v[48:51], v[148:151], v[184:187], 0
	s_waitcnt lgkmcnt(5)
	v_mfma_i32_16x16x64_i8 v[40:43], v[140:143], v[192:195], 0
	v_mfma_i32_16x16x64_i8 v[32:35], v[148:151], v[192:195], 0
	s_waitcnt lgkmcnt(3)
	v_mfma_i32_16x16x64_i8 v[24:27], v[140:143], v[202:205], 0
	v_mfma_i32_16x16x64_i8 v[16:19], v[148:151], v[202:205], 0
	s_waitcnt lgkmcnt(1)
	v_mfma_i32_16x16x64_i8 v[8:11], v[140:143], v[210:213], 0
	v_mfma_i32_16x16x64_i8 v[0:3], v[148:151], v[210:213], 0
	v_mfma_i32_16x16x64_i8 v[56:59], v[144:147], v[188:191], v[56:59]
	v_mfma_i32_16x16x64_i8 v[48:51], v[152:155], v[188:191], v[48:51]
	v_mfma_i32_16x16x64_i8 v[40:43], v[144:147], v[196:199], v[40:43]
	v_mfma_i32_16x16x64_i8 v[32:35], v[152:155], v[196:199], v[32:35]
	v_mfma_i32_16x16x64_i8 v[24:27], v[144:147], v[206:209], v[24:27]
	v_mfma_i32_16x16x64_i8 v[16:19], v[152:155], v[206:209], v[16:19]
	s_waitcnt lgkmcnt(0)
	v_mfma_i32_16x16x64_i8 v[8:11], v[144:147], v[214:217], v[8:11]
	v_mfma_i32_16x16x64_i8 v[0:3], v[152:155], v[214:217], v[0:3]
	s_setprio 0
	s_setprio 1
	v_mfma_i32_16x16x64_i8 v[60:63], v[156:159], v[184:187], 0
	v_mfma_i32_16x16x64_i8 v[52:55], v[164:167], v[184:187], 0
	v_mfma_i32_16x16x64_i8 v[44:47], v[156:159], v[192:195], 0
	v_mfma_i32_16x16x64_i8 v[36:39], v[164:167], v[192:195], 0
	v_mfma_i32_16x16x64_i8 v[28:31], v[156:159], v[202:205], 0
	v_mfma_i32_16x16x64_i8 v[20:23], v[164:167], v[202:205], 0
	v_mfma_i32_16x16x64_i8 v[12:15], v[156:159], v[210:213], 0
	v_mfma_i32_16x16x64_i8 v[4:7], v[164:167], v[210:213], 0
	v_mfma_i32_16x16x64_i8 v[60:63], v[160:163], v[188:191], v[60:63]
	v_mfma_i32_16x16x64_i8 v[52:55], v[180:183], v[188:191], v[52:55]
	v_mfma_i32_16x16x64_i8 v[44:47], v[160:163], v[196:199], v[44:47]
	v_mfma_i32_16x16x64_i8 v[36:39], v[180:183], v[196:199], v[36:39]
	v_mfma_i32_16x16x64_i8 v[28:31], v[160:163], v[206:209], v[28:31]
	v_mfma_i32_16x16x64_i8 v[20:23], v[180:183], v[206:209], v[20:23]
	v_mfma_i32_16x16x64_i8 v[12:15], v[160:163], v[214:217], v[12:15]
	v_mfma_i32_16x16x64_i8 v[4:7], v[180:183], v[214:217], v[4:7]
	s_setprio 0
	s_barrier
	v_add_u32_e32 v152, s56, v174
	v_add_u32_e32 v180, s57, v174
	ds_read_b128 v[140:143], v152
	ds_read_b128 v[144:147], v152 offset:1024
	ds_read_b128 v[148:151], v152 offset:2048
	ds_read_b128 v[152:155], v152 offset:3072
	ds_read_b128 v[156:159], v180
	ds_read_b128 v[160:163], v180 offset:1024
	ds_read_b128 v[164:167], v180 offset:2048
	ds_read_b128 v[180:183], v180 offset:3072
	ds_read_b128 v[184:187], v175 offset:32768
	ds_read_b128 v[188:191], v175 offset:33792
	ds_read_b128 v[192:195], v175 offset:34816
	ds_read_b128 v[196:199], v175 offset:35840
	ds_read_b128 v[202:205], v175 offset:36864
	ds_read_b128 v[206:209], v175 offset:37888
	ds_read_b128 v[210:213], v175 offset:38912
	ds_read_b128 v[214:217], v175 offset:39936
	s_mov_b32 m0, s35
	s_nop 4
	global_load_lds_dwordx4 v218, s[4:5]
	s_mov_b32 m0, s38
	s_nop 4
	global_load_lds_dwordx4 v220, s[4:5]
	s_waitcnt vmcnt(8)
	s_waitcnt lgkmcnt(0)
	s_barrier
	s_setprio 1
	s_waitcnt lgkmcnt(7)
	v_mfma_i32_16x16x64_i8 v[120:123], v[140:143], v[184:187], v[120:123]
	v_mfma_i32_16x16x64_i8 v[112:115], v[148:151], v[184:187], v[112:115]
	s_waitcnt lgkmcnt(5)
	v_mfma_i32_16x16x64_i8 v[104:107], v[140:143], v[192:195], v[104:107]
	v_mfma_i32_16x16x64_i8 v[96:99], v[148:151], v[192:195], v[96:99]
	s_waitcnt lgkmcnt(3)
	v_mfma_i32_16x16x64_i8 v[88:91], v[140:143], v[202:205], v[88:91]
	v_mfma_i32_16x16x64_i8 v[80:83], v[148:151], v[202:205], v[80:83]
	s_waitcnt lgkmcnt(1)
	v_mfma_i32_16x16x64_i8 v[72:75], v[140:143], v[210:213], v[72:75]
	v_mfma_i32_16x16x64_i8 v[64:67], v[148:151], v[210:213], v[64:67]
	v_mfma_i32_16x16x64_i8 v[120:123], v[144:147], v[188:191], v[120:123]
	v_mfma_i32_16x16x64_i8 v[112:115], v[152:155], v[188:191], v[112:115]
	v_mfma_i32_16x16x64_i8 v[104:107], v[144:147], v[196:199], v[104:107]
	v_mfma_i32_16x16x64_i8 v[96:99], v[152:155], v[196:199], v[96:99]
	v_mfma_i32_16x16x64_i8 v[88:91], v[144:147], v[206:209], v[88:91]
	v_mfma_i32_16x16x64_i8 v[80:83], v[152:155], v[206:209], v[80:83]
	s_waitcnt lgkmcnt(0)
	v_mfma_i32_16x16x64_i8 v[72:75], v[144:147], v[214:217], v[72:75]
	v_mfma_i32_16x16x64_i8 v[64:67], v[152:155], v[214:217], v[64:67]
	s_setprio 0
	s_setprio 1
	v_mfma_i32_16x16x64_i8 v[124:127], v[156:159], v[184:187], v[124:127]
	v_mfma_i32_16x16x64_i8 v[116:119], v[164:167], v[184:187], v[116:119]
	v_mfma_i32_16x16x64_i8 v[108:111], v[156:159], v[192:195], v[108:111]
	v_mfma_i32_16x16x64_i8 v[100:103], v[164:167], v[192:195], v[100:103]
	v_mfma_i32_16x16x64_i8 v[92:95], v[156:159], v[202:205], v[92:95]
	v_mfma_i32_16x16x64_i8 v[84:87], v[164:167], v[202:205], v[84:87]
	v_mfma_i32_16x16x64_i8 v[76:79], v[156:159], v[210:213], v[76:79]
	v_mfma_i32_16x16x64_i8 v[68:71], v[164:167], v[210:213], v[68:71]
	v_mfma_i32_16x16x64_i8 v[124:127], v[160:163], v[188:191], v[124:127]
	v_mfma_i32_16x16x64_i8 v[116:119], v[180:183], v[188:191], v[116:119]
	v_mfma_i32_16x16x64_i8 v[108:111], v[160:163], v[196:199], v[108:111]
	v_mfma_i32_16x16x64_i8 v[100:103], v[180:183], v[196:199], v[100:103]
	v_mfma_i32_16x16x64_i8 v[92:95], v[160:163], v[206:209], v[92:95]
	v_mfma_i32_16x16x64_i8 v[84:87], v[180:183], v[206:209], v[84:87]
	v_mfma_i32_16x16x64_i8 v[76:79], v[160:163], v[214:217], v[76:79]
	v_mfma_i32_16x16x64_i8 v[68:71], v[180:183], v[214:217], v[68:71]
	s_setprio 0
	s_barrier
	ds_read_b128 v[184:187], v175 offset:49152
	ds_read_b128 v[188:191], v175 offset:50176
	ds_read_b128 v[192:195], v175 offset:51200
	ds_read_b128 v[196:199], v175 offset:52224
	ds_read_b128 v[202:205], v175 offset:53248
	ds_read_b128 v[206:209], v175 offset:54272
	ds_read_b128 v[210:213], v175 offset:55296
	ds_read_b128 v[214:217], v175 offset:56320
	s_add_u32 s16, s25, s71
	s_addc_u32 s17, s26, 0
	s_mov_b32 m0, s47
	s_nop 4
	global_load_lds_dwordx4 v171, s[16:17]
	s_add_i32 s70, s70, 0x100080
	s_mov_b32 m0, s48
	s_nop 4
	global_load_lds_dwordx4 v173, s[16:17]
	s_add_u32 s16, s25, s70
	s_addc_u32 s17, s26, 0
	s_mov_b32 m0, s51
	s_nop 4
	global_load_lds_dwordx4 v171, s[16:17]
	s_mov_b32 m0, s52
	s_nop 4
	global_load_lds_dwordx4 v173, s[16:17]
	s_add_u32 s4, s4, 0x80
	s_addc_u32 s5, s5, 0
	s_mov_b32 m0, s49
	s_nop 4
	global_load_lds_dwordx4 v200, s[4:5]
	s_mov_b32 m0, s50
	s_nop 4
	global_load_lds_dwordx4 v219, s[4:5]
	s_waitcnt vmcnt(8)
	s_waitcnt lgkmcnt(0)
	s_barrier
	s_setprio 1
	s_waitcnt lgkmcnt(7)
	v_mfma_i32_16x16x64_i8 v[56:59], v[140:143], v[184:187], v[56:59]
	v_mfma_i32_16x16x64_i8 v[48:51], v[148:151], v[184:187], v[48:51]
	s_waitcnt lgkmcnt(5)
	v_mfma_i32_16x16x64_i8 v[40:43], v[140:143], v[192:195], v[40:43]
	v_mfma_i32_16x16x64_i8 v[32:35], v[148:151], v[192:195], v[32:35]
	s_waitcnt lgkmcnt(3)
	v_mfma_i32_16x16x64_i8 v[24:27], v[140:143], v[202:205], v[24:27]
	v_mfma_i32_16x16x64_i8 v[16:19], v[148:151], v[202:205], v[16:19]
	s_waitcnt lgkmcnt(1)
	v_mfma_i32_16x16x64_i8 v[8:11], v[140:143], v[210:213], v[8:11]
	v_mfma_i32_16x16x64_i8 v[0:3], v[148:151], v[210:213], v[0:3]
	v_mfma_i32_16x16x64_i8 v[56:59], v[144:147], v[188:191], v[56:59]
	v_mfma_i32_16x16x64_i8 v[48:51], v[152:155], v[188:191], v[48:51]
	v_mfma_i32_16x16x64_i8 v[40:43], v[144:147], v[196:199], v[40:43]
	v_mfma_i32_16x16x64_i8 v[32:35], v[152:155], v[196:199], v[32:35]
	v_mfma_i32_16x16x64_i8 v[24:27], v[144:147], v[206:209], v[24:27]
	v_mfma_i32_16x16x64_i8 v[16:19], v[152:155], v[206:209], v[16:19]
	s_waitcnt lgkmcnt(0)
	v_mfma_i32_16x16x64_i8 v[8:11], v[144:147], v[214:217], v[8:11]
	v_mfma_i32_16x16x64_i8 v[0:3], v[152:155], v[214:217], v[0:3]
	s_setprio 0
	s_setprio 1
	v_mfma_i32_16x16x64_i8 v[60:63], v[156:159], v[184:187], v[60:63]
	v_mfma_i32_16x16x64_i8 v[52:55], v[164:167], v[184:187], v[52:55]
	v_mfma_i32_16x16x64_i8 v[44:47], v[156:159], v[192:195], v[44:47]
	v_mfma_i32_16x16x64_i8 v[36:39], v[164:167], v[192:195], v[36:39]
	v_mfma_i32_16x16x64_i8 v[28:31], v[156:159], v[202:205], v[28:31]
	v_mfma_i32_16x16x64_i8 v[20:23], v[164:167], v[202:205], v[20:23]
	v_mfma_i32_16x16x64_i8 v[12:15], v[156:159], v[210:213], v[12:15]
	v_mfma_i32_16x16x64_i8 v[4:7], v[164:167], v[210:213], v[4:7]
	v_mfma_i32_16x16x64_i8 v[60:63], v[160:163], v[188:191], v[60:63]
	v_mfma_i32_16x16x64_i8 v[52:55], v[180:183], v[188:191], v[52:55]
	v_mfma_i32_16x16x64_i8 v[44:47], v[160:163], v[196:199], v[44:47]
	v_mfma_i32_16x16x64_i8 v[36:39], v[180:183], v[196:199], v[36:39]
	v_mfma_i32_16x16x64_i8 v[28:31], v[160:163], v[206:209], v[28:31]
	v_mfma_i32_16x16x64_i8 v[20:23], v[180:183], v[206:209], v[20:23]
	v_mfma_i32_16x16x64_i8 v[12:15], v[160:163], v[214:217], v[12:15]
	v_mfma_i32_16x16x64_i8 v[4:7], v[180:183], v[214:217], v[4:7]
	s_setprio 0
	s_barrier
	s_add_i32 s21, s21, 2
	s_mov_b64 s[16:17], s[14:15]

.LBB0_942:
	v_mbcnt_lo_u32_b32 v128, -1, 0
	v_mbcnt_hi_u32_b32 v128, -1, v128
	v_cvt_f32_i32_e32 v120, v120
	v_lshrrev_b32_e32 v129, 1, v128
	v_and_or_b32 v180, v129, 24, s46
	v_lshl_add_u32 v129, v180, 2, s20
	v_and_b32_e32 v181, 15, v128
	s_add_i32 s20, s20, s58
	v_add_u32_e32 v134, 0x20000, v129
	v_add_u32_e32 v129, 0x20400, v129
	v_lshl_add_u32 v128, v181, 2, s20
	ds_read_b128 v[130:133], v134
	ds_read_b128 v[136:139], v134 offset:16
	ds_read_b128 v[140:143], v129
	ds_read_b128 v[182:185], v129 offset:16
	ds_read_b128 v[186:189], v134 offset:512
	ds_read_b128 v[148:151], v129 offset:512
	ds_read_b128 v[190:193], v134 offset:528
	ds_read_b128 v[194:197], v129 offset:528
	v_add_u32_e32 v129, 0x20800, v128
	ds_read2_b32 v[166:167], v129 offset1:16
	ds_read2_b32 v[164:165], v129 offset0:32 offset1:48
	v_add_u32_e32 v128, 0x20a00, v128
	s_mov_b32 s4, 0xc01d265f
	s_mov_b32 s15, 0xc1898193
	s_mov_b32 s17, 0xc1c37b6f
	s_mov_b32 s16, 0xc0437b6f
	s_mov_b32 s14, 0x41929c93
	ds_read2_b32 v[162:163], v128 offset1:16
	ds_read2_b32 v[128:129], v128 offset0:32 offset1:48
	v_cvt_f32_i32_e32 v121, v121
	s_waitcnt lgkmcnt(9)
	v_pk_mul_f32 v[160:161], v[140:141], s[4:5] op_sel_hi:[1,0]
	v_pk_mul_f32 v[154:155], v[130:131], s[4:5] op_sel_hi:[1,0]
	v_mul_f32_e32 v120, v160, v120
	s_waitcnt lgkmcnt(8)
	v_pk_mul_f32 v[144:145], v[182:183], s[4:5] op_sel_hi:[1,0]
	s_waitcnt lgkmcnt(3)
	v_fma_f32 v183, v166, v120, v154
	v_cvt_f32_i32_e32 v120, v124
	v_pk_mul_f32 v[158:159], v[148:149], s[16:17] op_sel_hi:[1,0]
	v_pk_fma_f32 v[156:157], v[186:187], s[16:17], s[16:17] op_sel_hi:[1,0,0]
	v_pk_mul_f32 v[134:135], v[184:185], s[4:5] op_sel_hi:[1,0]
	v_mul_f32_e32 v120, v158, v120
	v_fma_f32 v184, v166, v120, v156
	v_max_f32_e64 v120, s15, s15
	v_max_f32_e32 v183, v183, v120
	v_exp_f32_e32 v185, v183
	v_mul_f32_e32 v121, v161, v121
	v_mov_b32_e32 v124, s17
	v_fma_f32 v121, v166, v121, v155
	v_add_f32_e32 v185, 1.0, v185
	v_rcp_f32_e32 v185, v185
	v_med3_f32 v184, v184, s14, v124
	v_max_f32_e32 v121, v121, v120
	v_cvt_f32_i32_e32 v125, v125
	v_mul_f32_e32 v183, v183, v185
	v_mul_f32_e32 v183, v184, v183
	v_exp_f32_e32 v184, v121
	v_cvt_f32_i32_e32 v122, v122
	v_pk_mul_f32 v[152:153], v[142:143], s[4:5] op_sel_hi:[1,0]
	v_pk_mul_f32 v[146:147], v[132:133], s[4:5] op_sel_hi:[1,0]
	v_add_f32_e32 v184, 1.0, v184
	v_rcp_f32_e32 v184, v184
	v_mul_f32_e32 v125, v159, v125
	v_mul_f32_e32 v122, v152, v122
	v_fma_f32 v125, v166, v125, v157
	v_fma_f32 v122, v166, v122, v146
	v_med3_f32 v125, v125, s14, v124
	v_mul_f32_e32 v121, v121, v184
	v_max_f32_e32 v122, v122, v120
	v_mul_f32_e32 v121, v125, v121
	v_cvt_f32_i32_e32 v125, v126
	v_exp_f32_e32 v126, v122
	v_cvt_f32_i32_e32 v123, v123
	v_pk_mul_f32 v[150:151], v[150:151], s[16:17] op_sel_hi:[1,0]
	v_pk_fma_f32 v[148:149], v[188:189], s[16:17], s[16:17] op_sel_hi:[1,0,0]
	v_add_f32_e32 v126, 1.0, v126
	v_rcp_f32_e32 v126, v126
	v_mul_f32_e32 v123, v153, v123
	v_fma_f32 v123, v166, v123, v147
	v_max_f32_e32 v123, v123, v120
	v_mul_f32_e32 v125, v150, v125
	v_mul_f32_e32 v122, v122, v126
	v_exp_f32_e32 v126, v123
	v_fma_f32 v125, v166, v125, v148
	v_med3_f32 v125, v125, s14, v124
	v_mul_f32_e32 v122, v125, v122
	v_cvt_f32_i32_e32 v125, v127
	v_cvt_f32_i32_e32 v112, v112
	v_add_f32_e32 v126, 1.0, v126
	v_rcp_f32_e32 v126, v126
	v_pk_mul_f32 v[130:131], v[138:139], s[4:5] op_sel_hi:[1,0]
	v_pk_mul_f32 v[138:139], v[136:137], s[4:5] op_sel_hi:[1,0]
	v_mul_f32_e32 v125, v151, v125
	v_mul_f32_e32 v112, v144, v112
	v_fma_f32 v125, v166, v125, v149
	v_fma_f32 v112, v166, v112, v138
	v_med3_f32 v125, v125, s14, v124
	v_mul_f32_e32 v123, v123, v126
	v_max_f32_e32 v112, v112, v120
	v_mul_f32_e32 v123, v125, v123
	v_exp_f32_e32 v125, v112
	v_cvt_f32_i32_e32 v116, v116
	v_pk_mul_f32 v[142:143], v[194:195], s[16:17] op_sel_hi:[1,0]
	v_pk_fma_f32 v[140:141], v[190:191], s[16:17], s[16:17] op_sel_hi:[1,0,0]
	v_add_f32_e32 v125, 1.0, v125
	v_rcp_f32_e32 v125, v125
	v_mul_f32_e32 v116, v142, v116
	v_fma_f32 v116, v166, v116, v140
	v_med3_f32 v116, v116, s14, v124
	v_mul_f32_e32 v112, v112, v125
	v_mul_f32_e32 v116, v116, v112
	v_cvt_f32_i32_e32 v112, v113
	v_cvt_f32_i32_e32 v113, v117
	v_pk_mul_f32 v[136:137], v[196:197], s[16:17] op_sel_hi:[1,0]
	v_pk_fma_f32 v[132:133], v[192:193], s[16:17], s[16:17] op_sel_hi:[1,0,0]
	v_mul_f32_e32 v112, v145, v112
	v_fma_f32 v112, v166, v112, v139
	v_max_f32_e32 v112, v112, v120
	v_exp_f32_e32 v117, v112
	v_mul_f32_e32 v113, v143, v113
	v_fma_f32 v113, v166, v113, v141
	v_med3_f32 v113, v113, s14, v124
	v_add_f32_e32 v117, 1.0, v117
	v_rcp_f32_e32 v117, v117
	v_cvt_f32_i32_e32 v104, v104
	s_add_u32 s4, s39, s33
	v_lshl_or_b32 v181, v181, 10, s59
	v_mul_f32_e32 v112, v112, v117
	v_mul_f32_e32 v117, v113, v112
	v_cvt_f32_i32_e32 v112, v114
	v_cvt_f32_i32_e32 v113, v118
	v_mul_f32_e32 v104, v160, v104
	v_fma_f32 v104, v167, v104, v154
	v_mul_f32_e32 v112, v134, v112
	v_fma_f32 v112, v166, v112, v130
	v_max_f32_e32 v112, v112, v120
	v_exp_f32_e32 v114, v112
	v_mul_f32_e32 v113, v136, v113
	v_fma_f32 v113, v166, v113, v132
	v_med3_f32 v113, v113, s14, v124
	v_add_f32_e32 v114, 1.0, v114
	v_rcp_f32_e32 v114, v114
	s_addc_u32 s5, s40, 0
	v_or_b32_e32 v182, v181, v180
	v_max_f32_e32 v104, v104, v120
	v_mul_f32_e32 v112, v112, v114
	v_mul_f32_e32 v114, v113, v112
	v_cvt_f32_i32_e32 v112, v115
	v_cvt_f32_i32_e32 v113, v119
	v_cvt_f32_i32_e32 v108, v108
	v_cvt_f32_i32_e32 v105, v105
	v_mul_f32_e32 v112, v135, v112
	v_fma_f32 v112, v166, v112, v131
	v_max_f32_e32 v112, v112, v120
	v_exp_f32_e32 v115, v112
	v_mul_f32_e32 v113, v137, v113
	v_fma_f32 v113, v166, v113, v133
	v_med3_f32 v113, v113, s14, v124
	v_add_f32_e32 v115, 1.0, v115
	v_rcp_f32_e32 v115, v115
	v_mul_f32_e32 v108, v158, v108
	v_mul_f32_e32 v105, v161, v105
	v_fma_f32 v108, v167, v108, v156
	v_mul_f32_e32 v112, v112, v115
	v_mul_f32_e32 v115, v113, v112
	v_mov_b32_e32 v112, v201
	v_mov_b32_e32 v113, v201
	v_cvt_pk_fp8_f32 v112, v183, v121
	v_cvt_pk_fp8_f32 v113, v116, v117
	v_fma_f32 v105, v167, v105, v155
	v_med3_f32 v108, v108, s14, v124
	v_cvt_pk_fp8_f32 v112, v122, v123 op_sel:[0,0,1]
	v_cvt_pk_fp8_f32 v113, v114, v115 op_sel:[0,0,1]
	v_max_f32_e32 v105, v105, v120
	v_cvt_f32_i32_e32 v106, v106
	v_cvt_f32_i32_e32 v107, v107
	global_store_dwordx2 v182, v[112:113], s[4:5]
	v_exp_f32_e32 v113, v104
	v_mul_f32_e32 v106, v152, v106
	v_fma_f32 v106, v167, v106, v146
	v_max_f32_e32 v106, v106, v120
	v_add_f32_e32 v113, 1.0, v113
	v_rcp_f32_e32 v113, v113
	v_mul_f32_e32 v107, v153, v107
	v_fma_f32 v107, v167, v107, v147
	v_max_f32_e32 v107, v107, v120
	v_mul_f32_e32 v104, v104, v113
	v_mul_f32_e32 v104, v108, v104
	v_cvt_f32_i32_e32 v108, v109
	v_exp_f32_e32 v109, v105
	v_cvt_f32_i32_e32 v96, v96
	v_cvt_f32_i32_e32 v100, v100
	v_mul_f32_e32 v108, v159, v108
	v_add_f32_e32 v109, 1.0, v109
	v_rcp_f32_e32 v109, v109
	v_fma_f32 v108, v167, v108, v157
	v_med3_f32 v108, v108, s14, v124
	v_mul_f32_e32 v96, v144, v96
	v_mul_f32_e32 v105, v105, v109
	v_exp_f32_e32 v109, v106
	v_mul_f32_e32 v105, v108, v105
	v_cvt_f32_i32_e32 v108, v110
	v_fma_f32 v96, v167, v96, v138
	v_add_f32_e32 v109, 1.0, v109
	v_rcp_f32_e32 v109, v109
	v_mul_f32_e32 v108, v150, v108
	v_fma_f32 v108, v167, v108, v148
	v_med3_f32 v108, v108, s14, v124
	v_mul_f32_e32 v106, v106, v109
	v_exp_f32_e32 v109, v107
	v_mul_f32_e32 v106, v108, v106
	v_cvt_f32_i32_e32 v108, v111
	v_max_f32_e32 v96, v96, v120
	v_add_f32_e32 v109, 1.0, v109
	v_rcp_f32_e32 v109, v109
	v_mul_f32_e32 v108, v151, v108
	v_fma_f32 v108, v167, v108, v149
	v_med3_f32 v108, v108, s14, v124
	v_mul_f32_e32 v107, v107, v109
	v_mul_f32_e32 v107, v108, v107
	v_exp_f32_e32 v108, v96
	v_mul_f32_e32 v100, v142, v100
	v_fma_f32 v100, v167, v100, v140
	v_med3_f32 v100, v100, s14, v124
	v_add_f32_e32 v108, 1.0, v108
	v_rcp_f32_e32 v108, v108
	v_cvt_f32_i32_e32 v88, v88
	v_or_b32_e32 v112, 0x4000, v182
	v_cvt_f32_i32_e32 v92, v92
	v_mul_f32_e32 v96, v96, v108
	v_mul_f32_e32 v100, v100, v96
	v_cvt_f32_i32_e32 v96, v97
	v_cvt_f32_i32_e32 v97, v101
	v_mul_f32_e32 v88, v160, v88
	s_waitcnt lgkmcnt(2)
	v_fma_f32 v88, v164, v88, v154
	v_mul_f32_e32 v96, v145, v96
	v_fma_f32 v96, v167, v96, v139
	v_max_f32_e32 v96, v96, v120
	v_exp_f32_e32 v101, v96
	v_mul_f32_e32 v97, v143, v97
	v_fma_f32 v97, v167, v97, v141
	v_med3_f32 v97, v97, s14, v124
	v_add_f32_e32 v101, 1.0, v101
	v_rcp_f32_e32 v101, v101
	v_max_f32_e32 v88, v88, v120
	v_cvt_f32_i32_e32 v89, v89
	v_mul_f32_e32 v92, v158, v92
	v_mul_f32_e32 v96, v96, v101
	v_mul_f32_e32 v101, v97, v96
	v_cvt_f32_i32_e32 v96, v98
	v_cvt_f32_i32_e32 v97, v102
	v_mul_f32_e32 v89, v161, v89
	v_fma_f32 v92, v164, v92, v156
	v_mul_f32_e32 v96, v134, v96
	v_fma_f32 v96, v167, v96, v130
	v_max_f32_e32 v96, v96, v120
	v_exp_f32_e32 v98, v96
	v_mul_f32_e32 v97, v136, v97
	v_fma_f32 v97, v167, v97, v132
	v_med3_f32 v97, v97, s14, v124
	v_add_f32_e32 v98, 1.0, v98
	v_rcp_f32_e32 v98, v98
	v_fma_f32 v89, v164, v89, v155
	v_med3_f32 v92, v92, s14, v124
	v_max_f32_e32 v89, v89, v120
	v_mul_f32_e32 v96, v96, v98
	v_mul_f32_e32 v98, v97, v96
	v_cvt_f32_i32_e32 v96, v99
	v_cvt_f32_i32_e32 v97, v103
	v_cvt_f32_i32_e32 v90, v90
	v_cvt_f32_i32_e32 v91, v91
	v_mul_f32_e32 v96, v135, v96
	v_fma_f32 v96, v167, v96, v131
	v_max_f32_e32 v96, v96, v120
	v_exp_f32_e32 v99, v96
	v_mul_f32_e32 v97, v137, v97
	v_fma_f32 v97, v167, v97, v133
	v_med3_f32 v97, v97, s14, v124
	v_add_f32_e32 v99, 1.0, v99
	v_rcp_f32_e32 v99, v99
	v_mul_f32_e32 v90, v152, v90
	v_fma_f32 v90, v164, v90, v146
	v_max_f32_e32 v90, v90, v120
	v_mul_f32_e32 v96, v96, v99
	v_mul_f32_e32 v99, v97, v96
	v_mov_b32_e32 v96, v201
	v_mov_b32_e32 v97, v201
	v_cvt_pk_fp8_f32 v96, v104, v105
	v_cvt_pk_fp8_f32 v97, v100, v101
	v_mul_f32_e32 v91, v153, v91
	v_fma_f32 v91, v164, v91, v147
	v_cvt_pk_fp8_f32 v96, v106, v107 op_sel:[0,0,1]
	v_cvt_pk_fp8_f32 v97, v98, v99 op_sel:[0,0,1]
	v_max_f32_e32 v91, v91, v120
	v_cvt_f32_i32_e32 v80, v80
	v_cvt_f32_i32_e32 v84, v84
	global_store_dwordx2 v112, v[96:97], s[4:5]
	v_exp_f32_e32 v97, v88
	v_mul_f32_e32 v80, v144, v80
	v_fma_f32 v80, v164, v80, v138
	v_max_f32_e32 v80, v80, v120
	v_add_f32_e32 v97, 1.0, v97
	v_rcp_f32_e32 v97, v97
	v_mul_f32_e32 v84, v142, v84
	v_fma_f32 v84, v164, v84, v140
	v_med3_f32 v84, v84, s14, v124
	v_mul_f32_e32 v88, v88, v97
	v_mul_f32_e32 v88, v92, v88
	v_cvt_f32_i32_e32 v92, v93
	v_exp_f32_e32 v93, v89
	v_cvt_f32_i32_e32 v72, v72
	v_or_b32_e32 v96, 0x8000, v182
	v_mul_f32_e32 v92, v159, v92
	v_add_f32_e32 v93, 1.0, v93
	v_rcp_f32_e32 v93, v93
	v_fma_f32 v92, v164, v92, v157
	v_med3_f32 v92, v92, s14, v124
	v_mul_f32_e32 v72, v160, v72
	v_mul_f32_e32 v89, v89, v93
	v_exp_f32_e32 v93, v90
	v_mul_f32_e32 v89, v92, v89
	v_cvt_f32_i32_e32 v92, v94
	v_fma_f32 v72, v165, v72, v154
	v_add_f32_e32 v93, 1.0, v93
	v_rcp_f32_e32 v93, v93
	v_mul_f32_e32 v92, v150, v92
	v_fma_f32 v92, v164, v92, v148
	v_med3_f32 v92, v92, s14, v124
	v_mul_f32_e32 v90, v90, v93
	v_exp_f32_e32 v93, v91
	v_mul_f32_e32 v90, v92, v90
	v_cvt_f32_i32_e32 v92, v95
	v_max_f32_e32 v72, v72, v120
	v_add_f32_e32 v93, 1.0, v93
	v_rcp_f32_e32 v93, v93
	v_mul_f32_e32 v92, v151, v92
	v_fma_f32 v92, v164, v92, v149
	v_med3_f32 v92, v92, s14, v124
	v_mul_f32_e32 v91, v91, v93
	v_mul_f32_e32 v91, v92, v91
	v_exp_f32_e32 v92, v80
	v_cvt_f32_i32_e32 v76, v76
	v_cvt_f32_i32_e32 v73, v73
	v_cvt_f32_i32_e32 v74, v74
	v_add_f32_e32 v92, 1.0, v92
	v_rcp_f32_e32 v92, v92
	v_mul_f32_e32 v76, v158, v76
	v_mul_f32_e32 v73, v161, v73
	v_fma_f32 v76, v165, v76, v156
	v_mul_f32_e32 v80, v80, v92
	v_mul_f32_e32 v84, v84, v80
	v_cvt_f32_i32_e32 v80, v81
	v_cvt_f32_i32_e32 v81, v85
	v_fma_f32 v73, v165, v73, v155
	v_med3_f32 v76, v76, s14, v124
	v_mul_f32_e32 v80, v145, v80
	v_fma_f32 v80, v164, v80, v139
	v_max_f32_e32 v80, v80, v120
	v_exp_f32_e32 v85, v80
	v_mul_f32_e32 v81, v143, v81
	v_fma_f32 v81, v164, v81, v141
	v_med3_f32 v81, v81, s14, v124
	v_add_f32_e32 v85, 1.0, v85
	v_rcp_f32_e32 v85, v85
	v_max_f32_e32 v73, v73, v120
	v_mul_f32_e32 v74, v152, v74
	v_fma_f32 v74, v165, v74, v146
	v_mul_f32_e32 v80, v80, v85
	v_mul_f32_e32 v85, v81, v80
	v_cvt_f32_i32_e32 v80, v82
	v_cvt_f32_i32_e32 v81, v86
	v_max_f32_e32 v74, v74, v120
	v_cvt_f32_i32_e32 v75, v75
	v_mul_f32_e32 v80, v134, v80
	v_fma_f32 v80, v164, v80, v130
	v_max_f32_e32 v80, v80, v120
	v_exp_f32_e32 v82, v80
	v_mul_f32_e32 v81, v136, v81
	v_fma_f32 v81, v164, v81, v132
	v_med3_f32 v81, v81, s14, v124
	v_add_f32_e32 v82, 1.0, v82
	v_rcp_f32_e32 v82, v82
	v_mul_f32_e32 v75, v153, v75
	v_fma_f32 v75, v165, v75, v147
	v_max_f32_e32 v75, v75, v120
	v_mul_f32_e32 v80, v80, v82
	v_mul_f32_e32 v82, v81, v80
	v_cvt_f32_i32_e32 v80, v83
	v_cvt_f32_i32_e32 v81, v87
	v_cvt_f32_i32_e32 v64, v64
	v_cvt_f32_i32_e32 v68, v68
	v_mul_f32_e32 v80, v135, v80
	v_fma_f32 v80, v164, v80, v131
	v_max_f32_e32 v80, v80, v120
	v_exp_f32_e32 v83, v80
	v_mul_f32_e32 v81, v137, v81
	v_fma_f32 v81, v164, v81, v133
	v_med3_f32 v81, v81, s14, v124
	v_add_f32_e32 v83, 1.0, v83
	v_rcp_f32_e32 v83, v83
	v_mul_f32_e32 v64, v144, v64
	v_fma_f32 v64, v165, v64, v138
	v_max_f32_e32 v64, v64, v120
	v_mul_f32_e32 v80, v80, v83
	v_mul_f32_e32 v83, v81, v80
	v_mov_b32_e32 v80, v201
	v_mov_b32_e32 v81, v201
	v_cvt_pk_fp8_f32 v80, v88, v89
	v_cvt_pk_fp8_f32 v81, v84, v85
	v_mul_f32_e32 v68, v142, v68
	v_fma_f32 v68, v165, v68, v140
	v_cvt_pk_fp8_f32 v80, v90, v91 op_sel:[0,0,1]
	v_cvt_pk_fp8_f32 v81, v82, v83 op_sel:[0,0,1]
	v_med3_f32 v68, v68, s14, v124
	v_cvt_f32_i32_e32 v56, v56
	v_cvt_f32_i32_e32 v60, v60
	global_store_dwordx2 v96, v[80:81], s[4:5]
	v_exp_f32_e32 v81, v72
	v_mul_f32_e32 v56, v160, v56
	s_waitcnt lgkmcnt(1)
	v_fma_f32 v56, v162, v56, v154
	v_max_f32_e32 v56, v56, v120
	v_add_f32_e32 v81, 1.0, v81
	v_rcp_f32_e32 v81, v81
	v_cvt_f32_i32_e32 v57, v57
	v_mul_f32_e32 v60, v158, v60
	v_fma_f32 v60, v162, v60, v156
	v_mul_f32_e32 v72, v72, v81
	v_mul_f32_e32 v72, v76, v72
	v_cvt_f32_i32_e32 v76, v77
	v_exp_f32_e32 v77, v73
	v_mul_f32_e32 v57, v161, v57
	v_fma_f32 v57, v162, v57, v155
	v_mul_f32_e32 v76, v159, v76
	v_add_f32_e32 v77, 1.0, v77
	v_rcp_f32_e32 v77, v77
	v_fma_f32 v76, v165, v76, v157
	v_med3_f32 v76, v76, s14, v124
	v_med3_f32 v60, v60, s14, v124
	v_mul_f32_e32 v73, v73, v77
	v_exp_f32_e32 v77, v74
	v_mul_f32_e32 v73, v76, v73
	v_cvt_f32_i32_e32 v76, v78
	v_max_f32_e32 v57, v57, v120
	v_add_f32_e32 v77, 1.0, v77
	v_rcp_f32_e32 v77, v77
	v_mul_f32_e32 v76, v150, v76
	v_fma_f32 v76, v165, v76, v148
	v_med3_f32 v76, v76, s14, v124
	v_mul_f32_e32 v74, v74, v77
	v_exp_f32_e32 v77, v75
	v_mul_f32_e32 v74, v76, v74
	v_cvt_f32_i32_e32 v76, v79
	v_cvt_f32_i32_e32 v58, v58
	v_add_f32_e32 v77, 1.0, v77
	v_rcp_f32_e32 v77, v77
	v_mul_f32_e32 v76, v151, v76
	v_fma_f32 v76, v165, v76, v149
	v_med3_f32 v76, v76, s14, v124
	v_mul_f32_e32 v75, v75, v77
	v_mul_f32_e32 v75, v76, v75
	v_exp_f32_e32 v76, v64
	v_mul_f32_e32 v58, v152, v58
	v_fma_f32 v58, v162, v58, v146
	v_max_f32_e32 v58, v58, v120
	v_add_f32_e32 v76, 1.0, v76
	v_rcp_f32_e32 v76, v76
	v_cvt_f32_i32_e32 v59, v59
	v_cvt_f32_i32_e32 v48, v48
	v_cvt_f32_i32_e32 v52, v52
	v_mul_f32_e32 v64, v64, v76
	v_mul_f32_e32 v68, v68, v64
	v_cvt_f32_i32_e32 v64, v65
	v_cvt_f32_i32_e32 v65, v69
	v_mul_f32_e32 v59, v153, v59
	v_fma_f32 v59, v162, v59, v147
	v_mul_f32_e32 v64, v145, v64
	v_fma_f32 v64, v165, v64, v139
	v_max_f32_e32 v64, v64, v120
	v_exp_f32_e32 v69, v64
	v_mul_f32_e32 v65, v143, v65
	v_fma_f32 v65, v165, v65, v141
	v_med3_f32 v65, v65, s14, v124
	v_add_f32_e32 v69, 1.0, v69
	v_rcp_f32_e32 v69, v69
	v_max_f32_e32 v59, v59, v120
	v_mul_f32_e32 v48, v144, v48
	v_fma_f32 v48, v162, v48, v138
	v_mul_f32_e32 v64, v64, v69
	v_mul_f32_e32 v69, v65, v64
	v_cvt_f32_i32_e32 v64, v66
	v_cvt_f32_i32_e32 v65, v70
	v_max_f32_e32 v48, v48, v120
	v_mul_f32_e32 v52, v142, v52
	v_mul_f32_e32 v64, v134, v64
	v_fma_f32 v64, v165, v64, v130
	v_max_f32_e32 v64, v64, v120
	v_exp_f32_e32 v66, v64
	v_mul_f32_e32 v65, v136, v65
	v_fma_f32 v65, v165, v65, v132
	v_med3_f32 v65, v65, s14, v124
	v_add_f32_e32 v66, 1.0, v66
	v_rcp_f32_e32 v66, v66
	v_fma_f32 v52, v162, v52, v140
	v_med3_f32 v52, v52, s14, v124
	v_cvt_f32_i32_e32 v40, v40
	v_mul_f32_e32 v64, v64, v66
	v_mul_f32_e32 v66, v65, v64
	v_cvt_f32_i32_e32 v64, v67
	v_cvt_f32_i32_e32 v65, v71
	v_or_b32_e32 v80, 0xc000, v182
	v_mul_f32_e32 v40, v160, v40
	v_mul_f32_e32 v64, v135, v64
	v_fma_f32 v64, v165, v64, v131
	v_max_f32_e32 v64, v64, v120
	v_exp_f32_e32 v67, v64
	v_mul_f32_e32 v65, v137, v65
	v_fma_f32 v65, v165, v65, v133
	v_med3_f32 v65, v65, s14, v124
	v_add_f32_e32 v67, 1.0, v67
	v_rcp_f32_e32 v67, v67
	v_fma_f32 v40, v163, v40, v154
	v_max_f32_e32 v40, v40, v120
	v_cvt_f32_i32_e32 v44, v44
	v_mul_f32_e32 v64, v64, v67
	v_mul_f32_e32 v67, v65, v64
	v_mov_b32_e32 v65, v201
	v_cvt_pk_fp8_f32 v65, v68, v69
	v_mov_b32_e32 v64, v201
	v_cvt_pk_fp8_f32 v64, v72, v73
	v_cvt_f32_i32_e32 v41, v41
	v_cvt_pk_fp8_f32 v65, v66, v67 op_sel:[0,0,1]
	v_exp_f32_e32 v66, v56
	v_cvt_pk_fp8_f32 v64, v74, v75 op_sel:[0,0,1]
	v_mul_f32_e32 v44, v158, v44
	v_mul_f32_e32 v41, v161, v41
	v_add_f32_e32 v66, 1.0, v66
	v_rcp_f32_e32 v66, v66
	global_store_dwordx2 v80, v[64:65], s[4:5]
	v_add_u32_e32 v64, v181, v180
	v_add_u32_e32 v65, 0x20000, v64
	v_mul_f32_e32 v56, v56, v66
	v_mul_f32_e32 v56, v60, v56
	v_cvt_f32_i32_e32 v60, v61
	v_exp_f32_e32 v61, v57
	v_fma_f32 v44, v163, v44, v156
	v_fma_f32 v41, v163, v41, v155
	v_mul_f32_e32 v60, v159, v60
	v_add_f32_e32 v61, 1.0, v61
	v_rcp_f32_e32 v61, v61
	v_fma_f32 v60, v162, v60, v157
	v_med3_f32 v60, v60, s14, v124
	v_med3_f32 v44, v44, s14, v124
	v_mul_f32_e32 v57, v57, v61
	v_exp_f32_e32 v61, v58
	v_mul_f32_e32 v57, v60, v57
	v_cvt_f32_i32_e32 v60, v62
	v_max_f32_e32 v41, v41, v120
	v_add_f32_e32 v61, 1.0, v61
	v_rcp_f32_e32 v61, v61
	v_mul_f32_e32 v60, v150, v60
	v_fma_f32 v60, v162, v60, v148
	v_med3_f32 v60, v60, s14, v124
	v_mul_f32_e32 v58, v58, v61
	v_exp_f32_e32 v61, v59
	v_mul_f32_e32 v58, v60, v58
	v_cvt_f32_i32_e32 v60, v63
	v_cvt_f32_i32_e32 v42, v42
	v_add_f32_e32 v61, 1.0, v61
	v_rcp_f32_e32 v61, v61
	v_mul_f32_e32 v60, v151, v60
	v_fma_f32 v60, v162, v60, v149
	v_med3_f32 v60, v60, s14, v124
	v_mul_f32_e32 v59, v59, v61
	v_mul_f32_e32 v59, v60, v59
	v_exp_f32_e32 v60, v48
	v_mul_f32_e32 v42, v152, v42
	v_fma_f32 v42, v163, v42, v146
	v_max_f32_e32 v42, v42, v120
	v_add_f32_e32 v60, 1.0, v60
	v_rcp_f32_e32 v60, v60
	v_cvt_f32_i32_e32 v43, v43
	v_cvt_f32_i32_e32 v32, v32
	v_cvt_f32_i32_e32 v36, v36
	v_mul_f32_e32 v48, v48, v60
	v_mul_f32_e32 v52, v52, v48
	v_cvt_f32_i32_e32 v48, v49
	v_cvt_f32_i32_e32 v49, v53
	v_mul_f32_e32 v43, v153, v43
	v_fma_f32 v43, v163, v43, v147
	v_mul_f32_e32 v48, v145, v48
	v_fma_f32 v48, v162, v48, v139
	v_max_f32_e32 v48, v48, v120
	v_exp_f32_e32 v53, v48
	v_mul_f32_e32 v49, v143, v49
	v_fma_f32 v49, v162, v49, v141
	v_med3_f32 v49, v49, s14, v124
	v_add_f32_e32 v53, 1.0, v53
	v_rcp_f32_e32 v53, v53
	v_max_f32_e32 v43, v43, v120
	v_mul_f32_e32 v32, v144, v32
	v_fma_f32 v32, v163, v32, v138
	v_mul_f32_e32 v48, v48, v53
	v_mul_f32_e32 v53, v49, v48
	v_cvt_f32_i32_e32 v48, v50
	v_cvt_f32_i32_e32 v49, v54
	v_max_f32_e32 v32, v32, v120
	v_mul_f32_e32 v36, v142, v36
	v_mul_f32_e32 v48, v134, v48
	v_fma_f32 v48, v162, v48, v130
	v_max_f32_e32 v48, v48, v120
	v_exp_f32_e32 v50, v48
	v_mul_f32_e32 v49, v136, v49
	v_fma_f32 v49, v162, v49, v132
	v_med3_f32 v49, v49, s14, v124
	v_add_f32_e32 v50, 1.0, v50
	v_rcp_f32_e32 v50, v50
	v_fma_f32 v36, v163, v36, v140
	v_med3_f32 v36, v36, s14, v124
	v_cvt_f32_i32_e32 v24, v24
	v_mul_f32_e32 v48, v48, v50
	v_mul_f32_e32 v50, v49, v48
	v_cvt_f32_i32_e32 v48, v51
	v_cvt_f32_i32_e32 v49, v55
	v_mul_f32_e32 v24, v160, v24
	s_waitcnt lgkmcnt(0)
	v_fma_f32 v24, v128, v24, v154
	v_mul_f32_e32 v48, v135, v48
	v_fma_f32 v48, v162, v48, v131
	v_max_f32_e32 v48, v48, v120
	v_exp_f32_e32 v51, v48
	v_mul_f32_e32 v49, v137, v49
	v_fma_f32 v49, v162, v49, v133
	v_med3_f32 v49, v49, s14, v124
	v_add_f32_e32 v51, 1.0, v51
	v_rcp_f32_e32 v51, v51
	v_max_f32_e32 v24, v24, v120
	v_cvt_f32_i32_e32 v28, v28
	v_cvt_f32_i32_e32 v25, v25
	v_mul_f32_e32 v48, v48, v51
	v_mul_f32_e32 v51, v49, v48
	v_mov_b32_e32 v48, v201
	v_mov_b32_e32 v49, v201
	v_cvt_pk_fp8_f32 v48, v56, v57
	v_cvt_pk_fp8_f32 v49, v52, v53
	v_mul_f32_e32 v28, v158, v28
	v_mul_f32_e32 v25, v161, v25
	v_cvt_pk_fp8_f32 v48, v58, v59 op_sel:[0,0,1]
	v_cvt_pk_fp8_f32 v49, v50, v51 op_sel:[0,0,1]
	v_fma_f32 v28, v128, v28, v156
	v_fma_f32 v25, v128, v25, v155
	v_med3_f32 v28, v28, s14, v124
	global_store_dwordx2 v65, v[48:49], s[4:5]
	v_exp_f32_e32 v49, v40
	v_add_u32_e32 v48, 0x24000, v64
	v_max_f32_e32 v25, v25, v120
	v_cvt_f32_i32_e32 v26, v26
	v_add_f32_e32 v49, 1.0, v49
	v_rcp_f32_e32 v49, v49
	v_cvt_f32_i32_e32 v27, v27
	v_mul_f32_e32 v26, v152, v26
	v_fma_f32 v26, v128, v26, v146
	v_mul_f32_e32 v40, v40, v49
	v_mul_f32_e32 v40, v44, v40
	v_cvt_f32_i32_e32 v44, v45
	v_exp_f32_e32 v45, v41
	v_max_f32_e32 v26, v26, v120
	v_mul_f32_e32 v27, v153, v27
	v_mul_f32_e32 v44, v159, v44
	v_add_f32_e32 v45, 1.0, v45
	v_rcp_f32_e32 v45, v45
	v_fma_f32 v44, v163, v44, v157
	v_med3_f32 v44, v44, s14, v124
	v_fma_f32 v27, v128, v27, v147
	v_mul_f32_e32 v41, v41, v45
	v_exp_f32_e32 v45, v42
	v_mul_f32_e32 v41, v44, v41
	v_cvt_f32_i32_e32 v44, v46
	v_max_f32_e32 v27, v27, v120
	v_add_f32_e32 v45, 1.0, v45
	v_rcp_f32_e32 v45, v45
	v_mul_f32_e32 v44, v150, v44
	v_fma_f32 v44, v163, v44, v148
	v_med3_f32 v44, v44, s14, v124
	v_mul_f32_e32 v42, v42, v45
	v_exp_f32_e32 v45, v43
	v_mul_f32_e32 v42, v44, v42
	v_cvt_f32_i32_e32 v44, v47
	v_cvt_f32_i32_e32 v16, v16
	v_add_f32_e32 v45, 1.0, v45
	v_rcp_f32_e32 v45, v45
	v_mul_f32_e32 v44, v151, v44
	v_fma_f32 v44, v163, v44, v149
	v_med3_f32 v44, v44, s14, v124
	v_mul_f32_e32 v43, v43, v45
	v_mul_f32_e32 v43, v44, v43
	v_exp_f32_e32 v44, v32
	v_mul_f32_e32 v16, v144, v16
	v_fma_f32 v16, v128, v16, v138
	v_max_f32_e32 v16, v16, v120
	v_add_f32_e32 v44, 1.0, v44
	v_rcp_f32_e32 v44, v44
	v_cvt_f32_i32_e32 v20, v20
	v_cvt_f32_i32_e32 v9, v9
	v_cvt_f32_i32_e32 v8, v8
	v_mul_f32_e32 v32, v32, v44
	v_mul_f32_e32 v36, v36, v32
	v_cvt_f32_i32_e32 v32, v33
	v_cvt_f32_i32_e32 v33, v37
	v_mul_f32_e32 v20, v142, v20
	v_fma_f32 v20, v128, v20, v140
	v_mul_f32_e32 v32, v145, v32
	v_fma_f32 v32, v163, v32, v139
	v_max_f32_e32 v32, v32, v120
	v_exp_f32_e32 v37, v32
	v_mul_f32_e32 v33, v143, v33
	v_fma_f32 v33, v163, v33, v141
	v_med3_f32 v33, v33, s14, v124
	v_add_f32_e32 v37, 1.0, v37
	v_rcp_f32_e32 v37, v37
	v_med3_f32 v20, v20, s14, v124
	v_mul_f32_e32 v9, v161, v9
	v_fmac_f32_e32 v155, v129, v9
	v_mul_f32_e32 v32, v32, v37
	v_mul_f32_e32 v37, v33, v32
	v_cvt_f32_i32_e32 v32, v34
	v_cvt_f32_i32_e32 v33, v38
	v_cvt_f32_i32_e32 v9, v13
	v_cvt_f32_i32_e32 v10, v10
	v_mul_f32_e32 v32, v134, v32
	v_fma_f32 v32, v163, v32, v130
	v_max_f32_e32 v32, v32, v120
	v_exp_f32_e32 v34, v32
	v_mul_f32_e32 v33, v136, v33
	v_fma_f32 v33, v163, v33, v132
	v_med3_f32 v33, v33, s14, v124
	v_add_f32_e32 v34, 1.0, v34
	v_rcp_f32_e32 v34, v34
	v_mul_f32_e32 v9, v159, v9
	v_mul_f32_e32 v8, v160, v8
	v_mul_f32_e32 v10, v152, v10
	v_mul_f32_e32 v32, v32, v34
	v_mul_f32_e32 v34, v33, v32
	v_cvt_f32_i32_e32 v32, v35
	v_cvt_f32_i32_e32 v33, v39
	v_fma_f32 v8, v129, v8, v154
	v_fma_f32 v10, v129, v10, v146
	v_mul_f32_e32 v32, v135, v32
	v_fma_f32 v32, v163, v32, v131
	v_max_f32_e32 v32, v32, v120
	v_exp_f32_e32 v35, v32
	v_mul_f32_e32 v33, v137, v33
	v_fma_f32 v33, v163, v33, v133
	v_med3_f32 v33, v33, s14, v124
	v_add_f32_e32 v35, 1.0, v35
	v_rcp_f32_e32 v35, v35
	v_cvt_f32_i32_e32 v11, v11
	v_max_f32_e32 v8, v8, v120
	v_max_f32_e32 v10, v10, v120
	v_mul_f32_e32 v32, v32, v35
	v_mul_f32_e32 v35, v33, v32
	v_mov_b32_e32 v32, v201
	v_mov_b32_e32 v33, v201
	v_cvt_pk_fp8_f32 v32, v40, v41
	v_cvt_pk_fp8_f32 v33, v36, v37
	v_mul_f32_e32 v11, v153, v11
	v_cvt_f32_i32_e32 v12, v12
	v_cvt_pk_fp8_f32 v32, v42, v43 op_sel:[0,0,1]
	v_cvt_pk_fp8_f32 v33, v34, v35 op_sel:[0,0,1]
	v_fmac_f32_e32 v147, v129, v11
	v_cvt_f32_i32_e32 v11, v15
	v_mul_f32_e32 v12, v158, v12
	global_store_dwordx2 v48, v[32:33], s[4:5]
	v_exp_f32_e32 v33, v24
	v_add_u32_e32 v32, 0x28000, v64
	v_mul_f32_e32 v11, v151, v11
	v_fma_f32 v12, v129, v12, v156
	v_add_f32_e32 v33, 1.0, v33
	v_rcp_f32_e32 v33, v33
	v_med3_f32 v12, v12, s14, v124
	v_cvt_f32_i32_e32 v0, v0
	v_cvt_f32_i32_e32 v4, v4
	v_mul_f32_e32 v24, v24, v33
	v_mul_f32_e32 v24, v28, v24
	v_cvt_f32_i32_e32 v28, v29
	v_exp_f32_e32 v29, v25
	v_mul_f32_e32 v0, v144, v0
	v_fma_f32 v0, v129, v0, v138
	v_mul_f32_e32 v28, v159, v28
	v_add_f32_e32 v29, 1.0, v29
	v_rcp_f32_e32 v29, v29
	v_fma_f32 v28, v128, v28, v157
	v_med3_f32 v28, v28, s14, v124
	v_fmac_f32_e32 v157, v129, v9
	v_mul_f32_e32 v25, v25, v29
	v_exp_f32_e32 v29, v26
	v_mul_f32_e32 v25, v28, v25
	v_cvt_f32_i32_e32 v28, v30
	v_max_f32_e32 v9, v155, v120
	v_add_f32_e32 v29, 1.0, v29
	v_rcp_f32_e32 v29, v29
	v_mul_f32_e32 v28, v150, v28
	v_fma_f32 v28, v128, v28, v148
	v_med3_f32 v28, v28, s14, v124
	v_mul_f32_e32 v26, v26, v29
	v_exp_f32_e32 v29, v27
	v_mul_f32_e32 v26, v28, v26
	v_cvt_f32_i32_e32 v28, v31
	v_exp_f32_e32 v13, v9
	v_add_f32_e32 v29, 1.0, v29
	v_rcp_f32_e32 v29, v29
	v_mul_f32_e32 v28, v151, v28
	v_fma_f32 v28, v128, v28, v149
	v_med3_f32 v28, v28, s14, v124
	v_mul_f32_e32 v27, v27, v29
	v_mul_f32_e32 v27, v28, v27
	v_exp_f32_e32 v28, v16
	v_add_f32_e32 v13, 1.0, v13
	v_rcp_f32_e32 v13, v13
	v_fmac_f32_e32 v149, v129, v11
	v_add_f32_e32 v28, 1.0, v28
	v_rcp_f32_e32 v28, v28
	v_mul_f32_e32 v9, v9, v13
	v_exp_f32_e32 v13, v10
	v_max_f32_e32 v11, v147, v120
	v_mul_f32_e32 v16, v16, v28
	v_mul_f32_e32 v20, v20, v16
	v_cvt_f32_i32_e32 v16, v17
	v_cvt_f32_i32_e32 v17, v21
	v_add_f32_e32 v13, 1.0, v13
	v_rcp_f32_e32 v13, v13
	v_mul_f32_e32 v16, v145, v16
	v_fma_f32 v16, v128, v16, v139
	v_max_f32_e32 v16, v16, v120
	v_exp_f32_e32 v21, v16
	v_mul_f32_e32 v17, v143, v17
	v_fma_f32 v17, v128, v17, v141
	v_med3_f32 v17, v17, s14, v124
	v_add_f32_e32 v21, 1.0, v21
	v_rcp_f32_e32 v21, v21
	v_mul_f32_e32 v10, v10, v13
	v_exp_f32_e32 v13, v11
	v_max_f32_e32 v0, v0, v120
	v_mul_f32_e32 v16, v16, v21
	v_mul_f32_e32 v21, v17, v16
	v_cvt_f32_i32_e32 v16, v18
	v_cvt_f32_i32_e32 v17, v22
	v_add_f32_e32 v13, 1.0, v13
	v_rcp_f32_e32 v13, v13
	v_mul_f32_e32 v16, v134, v16
	v_fma_f32 v16, v128, v16, v130
	v_max_f32_e32 v16, v16, v120
	v_exp_f32_e32 v18, v16
	v_mul_f32_e32 v17, v136, v17
	v_fma_f32 v17, v128, v17, v132
	v_med3_f32 v17, v17, s14, v124
	v_add_f32_e32 v18, 1.0, v18
	v_rcp_f32_e32 v18, v18
	v_mul_f32_e32 v11, v11, v13
	v_mul_f32_e32 v4, v142, v4
	v_fma_f32 v4, v129, v4, v140
	v_mul_f32_e32 v16, v16, v18
	v_mul_f32_e32 v18, v17, v16
	v_cvt_f32_i32_e32 v16, v19
	v_cvt_f32_i32_e32 v17, v23
	v_med3_f32 v4, v4, s14, v124
	s_andn2_b64 vcc, exec, s[12:13]
	v_mul_f32_e32 v16, v135, v16
	v_fma_f32 v16, v128, v16, v131
	v_max_f32_e32 v16, v16, v120
	v_exp_f32_e32 v19, v16
	v_mul_f32_e32 v17, v137, v17
	v_fma_f32 v17, v128, v17, v133
	v_med3_f32 v17, v17, s14, v124
	v_add_f32_e32 v19, 1.0, v19
	v_rcp_f32_e32 v19, v19
	s_nop 0
	v_mul_f32_e32 v16, v16, v19
	v_mul_f32_e32 v19, v17, v16
	v_mov_b32_e32 v16, v201
	v_mov_b32_e32 v17, v201
	v_cvt_pk_fp8_f32 v16, v24, v25
	v_cvt_pk_fp8_f32 v17, v20, v21
	v_cvt_pk_fp8_f32 v16, v26, v27 op_sel:[0,0,1]
	v_cvt_pk_fp8_f32 v17, v18, v19 op_sel:[0,0,1]
	global_store_dwordx2 v32, v[16:17], s[4:5]
	v_exp_f32_e32 v17, v8
	v_add_u32_e32 v16, 0x2c000, v64
	v_add_f32_e32 v17, 1.0, v17
	v_rcp_f32_e32 v17, v17
	s_nop 0
	v_mul_f32_e32 v8, v8, v17
	v_mul_f32_e32 v8, v12, v8
	v_med3_f32 v12, v157, s14, v124
	v_mul_f32_e32 v9, v12, v9
	v_cvt_f32_i32_e32 v12, v14
	v_mul_f32_e32 v12, v150, v12
	v_fma_f32 v12, v129, v12, v148
	v_med3_f32 v12, v12, s14, v124
	v_mul_f32_e32 v10, v12, v10
	v_med3_f32 v12, v149, s14, v124
	v_mul_f32_e32 v11, v12, v11
	v_exp_f32_e32 v12, v0
	s_nop 0
	v_add_f32_e32 v12, 1.0, v12
	v_rcp_f32_e32 v12, v12
	s_nop 0
	v_mul_f32_e32 v0, v0, v12
	v_mul_f32_e32 v4, v4, v0
	v_cvt_f32_i32_e32 v0, v1
	v_mul_f32_e32 v0, v145, v0
	v_fmac_f32_e32 v139, v129, v0
	v_cvt_f32_i32_e32 v0, v5
	v_mul_f32_e32 v0, v143, v0
	v_fmac_f32_e32 v141, v129, v0
	v_max_f32_e32 v0, v139, v120
	v_exp_f32_e32 v5, v0
	v_med3_f32 v1, v141, s14, v124
	v_add_f32_e32 v5, 1.0, v5
	v_rcp_f32_e32 v5, v5
	s_nop 0
	v_mul_f32_e32 v0, v0, v5
	v_mul_f32_e32 v5, v1, v0
	v_cvt_f32_i32_e32 v0, v2
	v_cvt_f32_i32_e32 v1, v6
	v_mul_f32_e32 v0, v134, v0
	v_fma_f32 v0, v129, v0, v130
	v_max_f32_e32 v0, v0, v120
	v_exp_f32_e32 v2, v0
	v_mul_f32_e32 v1, v136, v1
	v_fma_f32 v1, v129, v1, v132
	v_med3_f32 v1, v1, s14, v124
	v_add_f32_e32 v2, 1.0, v2
	v_rcp_f32_e32 v2, v2
	s_nop 0
	v_mul_f32_e32 v0, v0, v2
	v_mul_f32_e32 v2, v1, v0
	v_cvt_f32_i32_e32 v0, v3
	v_mul_f32_e32 v0, v135, v0
	v_fmac_f32_e32 v131, v129, v0
	v_cvt_f32_i32_e32 v0, v7
	v_mul_f32_e32 v0, v137, v0
	v_fmac_f32_e32 v133, v129, v0
	v_max_f32_e32 v0, v131, v120
	v_exp_f32_e32 v3, v0
	v_med3_f32 v1, v133, s14, v124
	v_add_f32_e32 v3, 1.0, v3
	v_rcp_f32_e32 v3, v3
	s_nop 0
	v_mul_f32_e32 v0, v0, v3
	v_mul_f32_e32 v3, v1, v0
	v_mov_b32_e32 v0, v201
	v_mov_b32_e32 v1, v201
	v_cvt_pk_fp8_f32 v0, v8, v9
	v_cvt_pk_fp8_f32 v1, v4, v5
	v_cvt_pk_fp8_f32 v0, v10, v11 op_sel:[0,0,1]
	v_cvt_pk_fp8_f32 v1, v2, v3 op_sel:[0,0,1]
	global_store_dwordx2 v16, v[0:1], s[4:5]
	s_mov_b64 s[4:5], -1
	s_cbranch_vccnz .LBB0_914
	s_andn2_b64 vcc, exec, s[8:9]
	s_cbranch_vccnz .LBB0_913
	s_barrier
	s_branch .LBB0_913
